# baseline (speedup 1.0000x reference)
_Z11pwconv_mfmaPKfPK15HIP_vector_typeIjLj4EES0_Pf:
	s_load_dwordx4 s[12:15], s[0:1], 0x0
	s_load_dwordx4 s[16:19], s[0:1], 0x10
	s_and_b32 s20, s2, 7
	s_lshr_b32 s21, s2, 3
	s_lshr_b32 s37, s20, 1
	s_and_b32 s36, s20, 1
	s_mul_i32 s36, s36, 31
	s_add_i32 s36, s36, s21
	s_lshr_b32 s21, s36, 1
	s_and_b32 s36, s36, 1
	s_lshl_b32 s37, s37, 1
	s_add_i32 s20, s37, s36
	v_lshrrev_b32_e32 v1, 6, v0
	v_and_b32_e32 v2, 63, v0
	s_nop 0
	v_readfirstlane_b32 s22, v1
	s_nop 3
	s_lshl_b32 s23, s20, 3
	s_add_i32 s23, s23, s22
	s_mul_i32 s24, s23, 0x439200
	s_mul_i32 s25, s21, 0x1f0
	s_add_u32 s24, s24, s25
	s_lshl_b32 s25, s21, 17
	s_lshl_b32 s26, s22, 13
	s_add_u32 s25, s25, s26
	s_mul_i32 s27, s20, 0x1e080
	s_mul_i32 s36, s21, 0x1f0
	s_add_u32 s27, s27, s36
	v_min_u32_e32 v10, 61, v2
	v_lshlrev_b32_e32 v3, 3, v10
	v_lshlrev_b32_e32 v4, 4, v2
	v_cmp_lt_u32_e32 vcc, 30, v10
	s_nop 1
	v_cndmask_b32_e64 v5, 0, 1, vcc
	v_mul_u32_u24_e32 v6, 31, v5
	v_sub_u32_e32 v6, v10, v6
	v_lshl_add_u32 v7, v1, 1, v5
	v_and_b32_e32 v8, 7, v6
	v_xor_b32_e32 v7, v7, v8
	v_lshlrev_b32_e32 v7, 4, v7
	v_lshl_add_u32 v5, v6, 12, v7
	s_lshl_b32 s36, s22, 2
	s_add_i32 s36, s36, 0
	s_and_b32 s36, s36, 7
	s_lshl_b32 s37, s22, 14
	s_add_i32 s37, s37, 0x0
	v_xor_b32_e32 v6, s36, v2
	v_lshlrev_b32_e32 v6, 4, v6
	v_add_u32_e32 v6, s37, v6
	s_lshl_b32 s36, s22, 2
	s_add_i32 s36, s36, 1
	s_and_b32 s36, s36, 7
	s_lshl_b32 s37, s22, 14
	s_add_i32 s37, s37, 0x1000
	v_xor_b32_e32 v7, s36, v2
	v_lshlrev_b32_e32 v7, 4, v7
	v_add_u32_e32 v7, s37, v7
	s_lshl_b32 s36, s22, 2
	s_add_i32 s36, s36, 2
	s_and_b32 s36, s36, 7
	s_lshl_b32 s37, s22, 14
	s_add_i32 s37, s37, 0x2000
	v_xor_b32_e32 v8, s36, v2
	v_lshlrev_b32_e32 v8, 4, v8
	v_add_u32_e32 v8, s37, v8
	s_lshl_b32 s36, s22, 2
	s_add_i32 s36, s36, 3
	s_and_b32 s36, s36, 7
	s_lshl_b32 s37, s22, 14
	s_add_i32 s37, s37, 0x3000
	v_xor_b32_e32 v9, s36, v2
	v_lshlrev_b32_e32 v9, 4, v9
	v_add_u32_e32 v9, s37, v9
	s_lshl_b32 s36, s22, 11
	s_add_i32 s36, s36, 0x20000
	v_add_u32_e32 v254, s36, v4
	s_add_i32 s37, s22, 1
	s_min_u32 s37, s37, 7
	s_lshl_b32 s37, s37, 11
	s_add_i32 s37, s37, 0x20000
	v_add_u32_e32 v255, s37, v4
	v_lshrrev_b32_e32 v10, 5, v0
	v_lshrrev_b32_e32 v11, 1, v10
	v_mul_u32_u24_e32 v11, 0x3c10, v11
	v_and_b32_e32 v10, 1, v10
	v_mul_u32_u24_e32 v10, 0xf8, v10
	v_add_u32_e32 v11, v11, v10
	v_and_b32_e32 v10, 31, v0
	v_lshl_add_u32 v11, v10, 3, v11
	v_add_u32_e32 v11, s27, v11
	v_cmp_eq_u32_e32 vcc, 31, v10
	v_mov_b32_e32 v10, 0x7f000000
	s_nop 1
	v_cndmask_b32_e32 v11, v11, v10, vcc
	s_waitcnt lgkmcnt(0)
	s_add_u32 s4, s12, s24
	s_addc_u32 s5, s13, 0
	s_and_b32 s5, s5, 0xffff
	s_sub_u32 s6, 0x10e48000, s24
	s_mov_b32 s7, 0x20000
	s_add_u32 s8, s14, s25
	s_addc_u32 s9, s15, 0
	s_and_b32 s9, s9, 0xffff
	s_sub_u32 s10, 0x400000, s25
	s_mov_b32 s11, 0x20000
	s_mov_b32 s28, s16
	s_and_b32 s29, s17, 0xffff
	s_mov_b32 s30, 0xf0400
	s_mov_b32 s31, 0x20000
	s_mov_b32 s32, s18
	s_and_b32 s33, s19, 0xffff
	s_mov_b32 s34, 0xf04000
	s_mov_b32 s35, 0x20000
	s_mov_b32 s40, 0x0
	s_mov_b32 s41, 0x21c90
	s_mov_b32 s42, 0x43920
	s_mov_b32 s43, 0x655b0
	s_mov_b32 s44, 0x87240
	s_mov_b32 s45, 0xa8ed0
	s_mov_b32 s46, 0xcab60
	s_mov_b32 s47, 0xec7f0
	buffer_load_dwordx2 v[44:45], v3, s[4:7], s40 offen nt
	buffer_load_dwordx2 v[46:47], v3, s[4:7], s41 offen nt
	buffer_load_dwordx2 v[48:49], v3, s[4:7], s42 offen nt
	buffer_load_dwordx2 v[50:51], v3, s[4:7], s43 offen nt
	buffer_load_dwordx2 v[52:53], v3, s[4:7], s44 offen nt
	buffer_load_dwordx2 v[54:55], v3, s[4:7], s45 offen nt
	buffer_load_dwordx2 v[56:57], v3, s[4:7], s46 offen nt
	buffer_load_dwordx2 v[58:59], v3, s[4:7], s47 offen nt
	s_mov_b32 s40, 0x10e480
	s_mov_b32 s41, 0x130110
	s_mov_b32 s42, 0x151da0
	s_mov_b32 s43, 0x173a30
	s_mov_b32 s44, 0x1956c0
	s_mov_b32 s45, 0x1b7350
	s_mov_b32 s46, 0x1d8fe0
	s_mov_b32 s47, 0x1fac70
	buffer_load_dwordx2 v[60:61], v3, s[4:7], s40 offen nt
	buffer_load_dwordx2 v[62:63], v3, s[4:7], s41 offen nt
	buffer_load_dwordx2 v[64:65], v3, s[4:7], s42 offen nt
	buffer_load_dwordx2 v[66:67], v3, s[4:7], s43 offen nt
	buffer_load_dwordx2 v[68:69], v3, s[4:7], s44 offen nt
	buffer_load_dwordx2 v[70:71], v3, s[4:7], s45 offen nt
	buffer_load_dwordx2 v[72:73], v3, s[4:7], s46 offen nt
	buffer_load_dwordx2 v[74:75], v3, s[4:7], s47 offen nt
	s_mov_b32 s40, 0x21c900
	s_mov_b32 s41, 0x23e590
	s_mov_b32 s42, 0x260220
	s_mov_b32 s43, 0x281eb0
	s_mov_b32 s44, 0x2a3b40
	s_mov_b32 s45, 0x2c57d0
	s_mov_b32 s46, 0x2e7460
	s_mov_b32 s47, 0x3090f0
	buffer_load_dwordx2 v[76:77], v3, s[4:7], s40 offen nt
	buffer_load_dwordx2 v[78:79], v3, s[4:7], s41 offen nt
	buffer_load_dwordx2 v[80:81], v3, s[4:7], s42 offen nt
	buffer_load_dwordx2 v[82:83], v3, s[4:7], s43 offen nt
	buffer_load_dwordx2 v[84:85], v3, s[4:7], s44 offen nt
	buffer_load_dwordx2 v[86:87], v3, s[4:7], s45 offen nt
	buffer_load_dwordx2 v[88:89], v3, s[4:7], s46 offen nt
	buffer_load_dwordx2 v[90:91], v3, s[4:7], s47 offen nt
	s_mov_b32 s40, 0x32ad80
	s_mov_b32 s41, 0x34ca10
	s_mov_b32 s42, 0x36e6a0
	s_mov_b32 s43, 0x390330
	s_mov_b32 s44, 0x3b1fc0
	s_mov_b32 s45, 0x3d3c50
	s_mov_b32 s46, 0x3f58e0
	s_mov_b32 s47, 0x417570
	buffer_load_dwordx2 v[92:93], v3, s[4:7], s40 offen nt
	buffer_load_dwordx2 v[94:95], v3, s[4:7], s41 offen nt
	buffer_load_dwordx2 v[96:97], v3, s[4:7], s42 offen nt
	buffer_load_dwordx2 v[98:99], v3, s[4:7], s43 offen nt
	buffer_load_dwordx2 v[100:101], v3, s[4:7], s44 offen nt
	buffer_load_dwordx2 v[102:103], v3, s[4:7], s45 offen nt
	buffer_load_dwordx2 v[104:105], v3, s[4:7], s46 offen nt
	buffer_load_dwordx2 v[106:107], v3, s[4:7], s47 offen nt
	buffer_load_dwordx2 v[252:253], v11, s[28:31], 0 offen
	s_mov_b32 s40, 0x0
	s_mov_b32 s41, 0x400
	s_mov_b32 s42, 0x800
	s_mov_b32 s43, 0xc00
	buffer_load_dwordx4 v[108:111], v4, s[8:11], s40 offen
	buffer_load_dwordx4 v[112:115], v4, s[8:11], s41 offen
	buffer_load_dwordx4 v[116:119], v4, s[8:11], s42 offen
	buffer_load_dwordx4 v[120:123], v4, s[8:11], s43 offen
	s_mov_b32 s40, 0x1000
	s_mov_b32 s41, 0x1400
	s_mov_b32 s42, 0x1800
	s_mov_b32 s43, 0x1c00
	buffer_load_dwordx4 v[124:127], v4, s[8:11], s40 offen
	buffer_load_dwordx4 v[128:131], v4, s[8:11], s41 offen
	buffer_load_dwordx4 v[132:135], v4, s[8:11], s42 offen
	buffer_load_dwordx4 v[136:139], v4, s[8:11], s43 offen
	s_mov_b32 s40, 0x10000
	s_mov_b32 s41, 0x10400
	s_mov_b32 s42, 0x10800
	s_mov_b32 s43, 0x10c00
	buffer_load_dwordx4 v[148:151], v4, s[8:11], s40 offen
	buffer_load_dwordx4 v[152:155], v4, s[8:11], s41 offen
	buffer_load_dwordx4 v[156:159], v4, s[8:11], s42 offen
	buffer_load_dwordx4 v[160:163], v4, s[8:11], s43 offen
	s_mov_b32 s40, 0x11000
	s_mov_b32 s41, 0x11400
	s_mov_b32 s42, 0x11800
	s_mov_b32 s43, 0x11c00
	buffer_load_dwordx4 v[164:167], v4, s[8:11], s40 offen
	buffer_load_dwordx4 v[168:171], v4, s[8:11], s41 offen
	buffer_load_dwordx4 v[172:175], v4, s[8:11], s42 offen
	buffer_load_dwordx4 v[176:179], v4, s[8:11], s43 offen
	s_waitcnt vmcnt(41)
	v_cvt_pkrtz_f16_f32 v12, v44, v46
	v_cvt_pkrtz_f16_f32 v13, v48, v50
	v_cvt_pkrtz_f16_f32 v14, v52, v54
	v_cvt_pkrtz_f16_f32 v15, v56, v58
	v_cvt_pkrtz_f16_f32 v16, v45, v47
	v_cvt_pkrtz_f16_f32 v17, v49, v51
	v_cvt_pkrtz_f16_f32 v18, v53, v55
	v_cvt_pkrtz_f16_f32 v19, v57, v59
	ds_write_b128 v5, v[12:15] offset:0
	ds_write_b128 v5, v[16:19] offset:2048
	s_waitcnt vmcnt(33)
	v_cvt_pkrtz_f16_f32 v12, v60, v62
	v_cvt_pkrtz_f16_f32 v13, v64, v66
	v_cvt_pkrtz_f16_f32 v14, v68, v70
	v_cvt_pkrtz_f16_f32 v15, v72, v74
	v_cvt_pkrtz_f16_f32 v16, v61, v63
	v_cvt_pkrtz_f16_f32 v17, v65, v67
	v_cvt_pkrtz_f16_f32 v18, v69, v71
	v_cvt_pkrtz_f16_f32 v19, v73, v75
	s_mov_b32 s40, 0x3c10
	s_mov_b32 s41, 0x258a0
	s_mov_b32 s42, 0x47530
	s_mov_b32 s43, 0x691c0
	s_mov_b32 s44, 0x8ae50
	s_mov_b32 s45, 0xacae0
	s_mov_b32 s46, 0xce770
	s_mov_b32 s47, 0xf0400
	buffer_load_dwordx2 v[44:45], v3, s[4:7], s40 offen nt
	buffer_load_dwordx2 v[46:47], v3, s[4:7], s41 offen nt
	buffer_load_dwordx2 v[48:49], v3, s[4:7], s42 offen nt
	buffer_load_dwordx2 v[50:51], v3, s[4:7], s43 offen nt
	buffer_load_dwordx2 v[52:53], v3, s[4:7], s44 offen nt
	buffer_load_dwordx2 v[54:55], v3, s[4:7], s45 offen nt
	buffer_load_dwordx2 v[56:57], v3, s[4:7], s46 offen nt
	buffer_load_dwordx2 v[58:59], v3, s[4:7], s47 offen nt
	ds_write_b128 v5, v[12:15] offset:256
	ds_write_b128 v5, v[16:19] offset:2304
	s_waitcnt vmcnt(33)
	v_cvt_pkrtz_f16_f32 v12, v76, v78
	v_cvt_pkrtz_f16_f32 v13, v80, v82
	v_cvt_pkrtz_f16_f32 v14, v84, v86
	v_cvt_pkrtz_f16_f32 v15, v88, v90
	v_cvt_pkrtz_f16_f32 v16, v77, v79
	v_cvt_pkrtz_f16_f32 v17, v81, v83
	v_cvt_pkrtz_f16_f32 v18, v85, v87
	v_cvt_pkrtz_f16_f32 v19, v89, v91
	s_mov_b32 s40, 0x112090
	s_mov_b32 s41, 0x133d20
	s_mov_b32 s42, 0x1559b0
	s_mov_b32 s43, 0x177640
	s_mov_b32 s44, 0x1992d0
	s_mov_b32 s45, 0x1baf60
	s_mov_b32 s46, 0x1dcbf0
	s_mov_b32 s47, 0x1fe880
	buffer_load_dwordx2 v[60:61], v3, s[4:7], s40 offen nt
	buffer_load_dwordx2 v[62:63], v3, s[4:7], s41 offen nt
	buffer_load_dwordx2 v[64:65], v3, s[4:7], s42 offen nt
	buffer_load_dwordx2 v[66:67], v3, s[4:7], s43 offen nt
	buffer_load_dwordx2 v[68:69], v3, s[4:7], s44 offen nt
	buffer_load_dwordx2 v[70:71], v3, s[4:7], s45 offen nt
	buffer_load_dwordx2 v[72:73], v3, s[4:7], s46 offen nt
	buffer_load_dwordx2 v[74:75], v3, s[4:7], s47 offen nt
	ds_write_b128 v5, v[12:15] offset:512
	ds_write_b128 v5, v[16:19] offset:2560
	s_waitcnt vmcnt(33)
	v_cvt_pkrtz_f16_f32 v12, v92, v94
	v_cvt_pkrtz_f16_f32 v13, v96, v98
	v_cvt_pkrtz_f16_f32 v14, v100, v102
	v_cvt_pkrtz_f16_f32 v15, v104, v106
	v_cvt_pkrtz_f16_f32 v16, v93, v95
	v_cvt_pkrtz_f16_f32 v17, v97, v99
	v_cvt_pkrtz_f16_f32 v18, v101, v103
	v_cvt_pkrtz_f16_f32 v19, v105, v107
	s_mov_b32 s40, 0x220510
	s_mov_b32 s41, 0x2421a0
	s_mov_b32 s42, 0x263e30
	s_mov_b32 s43, 0x285ac0
	s_mov_b32 s44, 0x2a7750
	s_mov_b32 s45, 0x2c93e0
	s_mov_b32 s46, 0x2eb070
	s_mov_b32 s47, 0x30cd00
	buffer_load_dwordx2 v[76:77], v3, s[4:7], s40 offen nt
	buffer_load_dwordx2 v[78:79], v3, s[4:7], s41 offen nt
	buffer_load_dwordx2 v[80:81], v3, s[4:7], s42 offen nt
	buffer_load_dwordx2 v[82:83], v3, s[4:7], s43 offen nt
	buffer_load_dwordx2 v[84:85], v3, s[4:7], s44 offen nt
	buffer_load_dwordx2 v[86:87], v3, s[4:7], s45 offen nt
	buffer_load_dwordx2 v[88:89], v3, s[4:7], s46 offen nt
	buffer_load_dwordx2 v[90:91], v3, s[4:7], s47 offen nt
	ds_write_b128 v5, v[12:15] offset:768
	ds_write_b128 v5, v[16:19] offset:2816
	s_waitcnt vmcnt(24)
	ds_write_b128 v254, v[108:111] offset:0
	ds_write_b128 v254, v[112:115] offset:1024
	ds_write_b128 v254, v[148:151] offset:16384
	ds_write_b128 v254, v[152:155] offset:17408
	s_waitcnt lgkmcnt(0)
	s_barrier
	ds_read_b128 v[140:143], v255 offset:0
	ds_read_b128 v[144:147], v255 offset:1024
	ds_read_b128 v[180:183], v255 offset:16384
	ds_read_b128 v[184:187], v255 offset:17408
	ds_read_b128 v[12:15], v6 offset:0
	ds_read_b128 v[16:19], v6 offset:2048
	ds_read_b128 v[20:23], v7 offset:0
	ds_read_b128 v[24:27], v7 offset:2048
	ds_read_b128 v[28:31], v8 offset:0
	ds_read_b128 v[32:35], v8 offset:2048
	ds_read_b128 v[36:39], v9 offset:0
	ds_read_b128 v[40:43], v9 offset:2048
	s_waitcnt lgkmcnt(7)
	v_mfma_f32_16x16x32_f16 v[188:191], v[108:111], v[12:15], 0
	v_mfma_f32_16x16x32_f16 v[220:223], v[148:151], v[12:15], 0
	s_waitcnt lgkmcnt(6)
	v_mfma_f32_16x16x32_f16 v[192:195], v[112:115], v[16:19], 0
	v_mfma_f32_16x16x32_f16 v[224:227], v[152:155], v[16:19], 0
	s_waitcnt lgkmcnt(5)
	v_mfma_f32_16x16x32_f16 v[196:199], v[116:119], v[20:23], 0
	v_mfma_f32_16x16x32_f16 v[228:231], v[156:159], v[20:23], 0
	s_waitcnt lgkmcnt(4)
	v_mfma_f32_16x16x32_f16 v[200:203], v[120:123], v[24:27], 0
	v_mfma_f32_16x16x32_f16 v[232:235], v[160:163], v[24:27], 0
	s_waitcnt lgkmcnt(3)
	v_mfma_f32_16x16x32_f16 v[204:207], v[124:127], v[28:31], 0
	v_mfma_f32_16x16x32_f16 v[236:239], v[164:167], v[28:31], 0
	s_waitcnt lgkmcnt(2)
	v_mfma_f32_16x16x32_f16 v[208:211], v[128:131], v[32:35], 0
	v_mfma_f32_16x16x32_f16 v[240:243], v[168:171], v[32:35], 0
	s_waitcnt lgkmcnt(1)
	v_mfma_f32_16x16x32_f16 v[212:215], v[132:135], v[36:39], 0
	v_mfma_f32_16x16x32_f16 v[244:247], v[172:175], v[36:39], 0
	s_waitcnt lgkmcnt(0)
	v_mfma_f32_16x16x32_f16 v[216:219], v[136:139], v[40:43], 0
	v_mfma_f32_16x16x32_f16 v[248:251], v[176:179], v[40:43], 0
	s_mov_b32 s40, 0x32e990
	s_mov_b32 s41, 0x350620
	s_mov_b32 s42, 0x3722b0
	s_mov_b32 s43, 0x393f40
	s_mov_b32 s44, 0x3b5bd0
	s_mov_b32 s45, 0x3d7860
	s_mov_b32 s46, 0x3f94f0
	s_mov_b32 s47, 0x41b180
	buffer_load_dwordx2 v[92:93], v3, s[4:7], s40 offen nt
	buffer_load_dwordx2 v[94:95], v3, s[4:7], s41 offen nt
	buffer_load_dwordx2 v[96:97], v3, s[4:7], s42 offen nt
	buffer_load_dwordx2 v[98:99], v3, s[4:7], s43 offen nt
	buffer_load_dwordx2 v[100:101], v3, s[4:7], s44 offen nt
	buffer_load_dwordx2 v[102:103], v3, s[4:7], s45 offen nt
	buffer_load_dwordx2 v[104:105], v3, s[4:7], s46 offen nt
	buffer_load_dwordx2 v[106:107], v3, s[4:7], s47 offen nt
	s_waitcnt vmcnt(24)
	v_cvt_pkrtz_f16_f32 v12, v44, v46
	v_cvt_pkrtz_f16_f32 v13, v48, v50
	v_cvt_pkrtz_f16_f32 v14, v52, v54
	v_cvt_pkrtz_f16_f32 v15, v56, v58
	v_cvt_pkrtz_f16_f32 v16, v45, v47
	v_cvt_pkrtz_f16_f32 v17, v49, v51
	v_cvt_pkrtz_f16_f32 v18, v53, v55
	v_cvt_pkrtz_f16_f32 v19, v57, v59
	ds_write_b128 v5, v[12:15] offset:1024
	ds_write_b128 v5, v[16:19] offset:3072
	s_waitcnt vmcnt(16)
	v_cvt_pkrtz_f16_f32 v12, v60, v62
	v_cvt_pkrtz_f16_f32 v13, v64, v66
	v_cvt_pkrtz_f16_f32 v14, v68, v70
	v_cvt_pkrtz_f16_f32 v15, v72, v74
	v_cvt_pkrtz_f16_f32 v16, v61, v63
	v_cvt_pkrtz_f16_f32 v17, v65, v67
	v_cvt_pkrtz_f16_f32 v18, v69, v71
	v_cvt_pkrtz_f16_f32 v19, v73, v75
	s_mov_b32 s40, 0x7820
	s_mov_b32 s41, 0x294b0
	s_mov_b32 s42, 0x4b140
	s_mov_b32 s43, 0x6cdd0
	s_mov_b32 s44, 0x8ea60
	s_mov_b32 s45, 0xb06f0
	s_mov_b32 s46, 0xd2380
	s_mov_b32 s47, 0xf4010
	buffer_load_dwordx2 v[44:45], v3, s[4:7], s40 offen nt
	buffer_load_dwordx2 v[46:47], v3, s[4:7], s41 offen nt
	buffer_load_dwordx2 v[48:49], v3, s[4:7], s42 offen nt
	buffer_load_dwordx2 v[50:51], v3, s[4:7], s43 offen nt
	buffer_load_dwordx2 v[52:53], v3, s[4:7], s44 offen nt
	buffer_load_dwordx2 v[54:55], v3, s[4:7], s45 offen nt
	buffer_load_dwordx2 v[56:57], v3, s[4:7], s46 offen nt
	buffer_load_dwordx2 v[58:59], v3, s[4:7], s47 offen nt
	ds_write_b128 v5, v[12:15] offset:1280
	ds_write_b128 v5, v[16:19] offset:3328
	s_waitcnt vmcnt(16)
	v_cvt_pkrtz_f16_f32 v12, v76, v78
	v_cvt_pkrtz_f16_f32 v13, v80, v82
	v_cvt_pkrtz_f16_f32 v14, v84, v86
	v_cvt_pkrtz_f16_f32 v15, v88, v90
	v_cvt_pkrtz_f16_f32 v16, v77, v79
	v_cvt_pkrtz_f16_f32 v17, v81, v83
	v_cvt_pkrtz_f16_f32 v18, v85, v87
	v_cvt_pkrtz_f16_f32 v19, v89, v91
	s_mov_b32 s40, 0x115ca0
	s_mov_b32 s41, 0x137930
	s_mov_b32 s42, 0x1595c0
	s_mov_b32 s43, 0x17b250
	s_mov_b32 s44, 0x19cee0
	s_mov_b32 s45, 0x1beb70
	s_mov_b32 s46, 0x1e0800
	s_mov_b32 s47, 0x202490
	buffer_load_dwordx2 v[60:61], v3, s[4:7], s40 offen nt
	buffer_load_dwordx2 v[62:63], v3, s[4:7], s41 offen nt
	buffer_load_dwordx2 v[64:65], v3, s[4:7], s42 offen nt
	buffer_load_dwordx2 v[66:67], v3, s[4:7], s43 offen nt
	buffer_load_dwordx2 v[68:69], v3, s[4:7], s44 offen nt
	buffer_load_dwordx2 v[70:71], v3, s[4:7], s45 offen nt
	buffer_load_dwordx2 v[72:73], v3, s[4:7], s46 offen nt
	buffer_load_dwordx2 v[74:75], v3, s[4:7], s47 offen nt
	ds_write_b128 v5, v[12:15] offset:1536
	ds_write_b128 v5, v[16:19] offset:3584
	s_waitcnt vmcnt(16)
	v_cvt_pkrtz_f16_f32 v12, v92, v94
	v_cvt_pkrtz_f16_f32 v13, v96, v98
	v_cvt_pkrtz_f16_f32 v14, v100, v102
	v_cvt_pkrtz_f16_f32 v15, v104, v106
	v_cvt_pkrtz_f16_f32 v16, v93, v95
	v_cvt_pkrtz_f16_f32 v17, v97, v99
	v_cvt_pkrtz_f16_f32 v18, v101, v103
	v_cvt_pkrtz_f16_f32 v19, v105, v107
	s_mov_b32 s40, 0x224120
	s_mov_b32 s41, 0x245db0
	s_mov_b32 s42, 0x267a40
	s_mov_b32 s43, 0x2896d0
	s_mov_b32 s44, 0x2ab360
	s_mov_b32 s45, 0x2ccff0
	s_mov_b32 s46, 0x2eec80
	s_mov_b32 s47, 0x310910
	buffer_load_dwordx2 v[76:77], v3, s[4:7], s40 offen nt
	buffer_load_dwordx2 v[78:79], v3, s[4:7], s41 offen nt
	buffer_load_dwordx2 v[80:81], v3, s[4:7], s42 offen nt
	buffer_load_dwordx2 v[82:83], v3, s[4:7], s43 offen nt
	buffer_load_dwordx2 v[84:85], v3, s[4:7], s44 offen nt
	buffer_load_dwordx2 v[86:87], v3, s[4:7], s45 offen nt
	buffer_load_dwordx2 v[88:89], v3, s[4:7], s46 offen nt
	buffer_load_dwordx2 v[90:91], v3, s[4:7], s47 offen nt
	ds_write_b128 v5, v[12:15] offset:1792
	ds_write_b128 v5, v[16:19] offset:3840
	s_waitcnt lgkmcnt(0)
	s_barrier
	ds_read_b128 v[12:15], v6 offset:1024
	ds_read_b128 v[16:19], v6 offset:3072
	ds_read_b128 v[20:23], v7 offset:1024
	ds_read_b128 v[24:27], v7 offset:3072
	ds_read_b128 v[28:31], v8 offset:1024
	ds_read_b128 v[32:35], v8 offset:3072
	ds_read_b128 v[36:39], v9 offset:1024
	ds_read_b128 v[40:43], v9 offset:3072
	s_waitcnt lgkmcnt(7)
	v_mfma_f32_16x16x32_f16 v[188:191], v[112:115], v[12:15], v[188:191]
	v_mfma_f32_16x16x32_f16 v[220:223], v[152:155], v[12:15], v[220:223]
	s_waitcnt lgkmcnt(6)
	v_mfma_f32_16x16x32_f16 v[192:195], v[116:119], v[16:19], v[192:195]
	v_mfma_f32_16x16x32_f16 v[224:227], v[156:159], v[16:19], v[224:227]
	s_waitcnt lgkmcnt(5)
	v_mfma_f32_16x16x32_f16 v[196:199], v[120:123], v[20:23], v[196:199]
	v_mfma_f32_16x16x32_f16 v[228:231], v[160:163], v[20:23], v[228:231]
	s_waitcnt lgkmcnt(4)
	v_mfma_f32_16x16x32_f16 v[200:203], v[124:127], v[24:27], v[200:203]
	v_mfma_f32_16x16x32_f16 v[232:235], v[164:167], v[24:27], v[232:235]
	s_waitcnt lgkmcnt(3)
	v_mfma_f32_16x16x32_f16 v[204:207], v[128:131], v[28:31], v[204:207]
	v_mfma_f32_16x16x32_f16 v[236:239], v[168:171], v[28:31], v[236:239]
	s_waitcnt lgkmcnt(2)
	v_mfma_f32_16x16x32_f16 v[208:211], v[132:135], v[32:35], v[208:211]
	v_mfma_f32_16x16x32_f16 v[240:243], v[172:175], v[32:35], v[240:243]
	s_waitcnt lgkmcnt(1)
	v_mfma_f32_16x16x32_f16 v[212:215], v[136:139], v[36:39], v[212:215]
	v_mfma_f32_16x16x32_f16 v[244:247], v[176:179], v[36:39], v[244:247]
	s_waitcnt lgkmcnt(0)
	v_mfma_f32_16x16x32_f16 v[216:219], v[140:143], v[40:43], v[216:219]
	v_mfma_f32_16x16x32_f16 v[248:251], v[180:183], v[40:43], v[248:251]
	s_mov_b32 s40, 0x3325a0
	s_mov_b32 s41, 0x354230
	s_mov_b32 s42, 0x375ec0
	s_mov_b32 s43, 0x397b50
	s_mov_b32 s44, 0x3b97e0
	s_mov_b32 s45, 0x3db470
	s_mov_b32 s46, 0x3fd100
	s_mov_b32 s47, 0x41ed90
	buffer_load_dwordx2 v[92:93], v3, s[4:7], s40 offen nt
	buffer_load_dwordx2 v[94:95], v3, s[4:7], s41 offen nt
	buffer_load_dwordx2 v[96:97], v3, s[4:7], s42 offen nt
	buffer_load_dwordx2 v[98:99], v3, s[4:7], s43 offen nt
	buffer_load_dwordx2 v[100:101], v3, s[4:7], s44 offen nt
	buffer_load_dwordx2 v[102:103], v3, s[4:7], s45 offen nt
	buffer_load_dwordx2 v[104:105], v3, s[4:7], s46 offen nt
	buffer_load_dwordx2 v[106:107], v3, s[4:7], s47 offen nt
	s_waitcnt vmcnt(24)
	v_cvt_pkrtz_f16_f32 v12, v44, v46
	v_cvt_pkrtz_f16_f32 v13, v48, v50
	v_cvt_pkrtz_f16_f32 v14, v52, v54
	v_cvt_pkrtz_f16_f32 v15, v56, v58
	v_cvt_pkrtz_f16_f32 v16, v45, v47
	v_cvt_pkrtz_f16_f32 v17, v49, v51
	v_cvt_pkrtz_f16_f32 v18, v53, v55
	v_cvt_pkrtz_f16_f32 v19, v57, v59
	ds_write_b128 v5, v[12:15] offset:0
	ds_write_b128 v5, v[16:19] offset:2048
	s_waitcnt vmcnt(16)
	v_cvt_pkrtz_f16_f32 v12, v60, v62
	v_cvt_pkrtz_f16_f32 v13, v64, v66
	v_cvt_pkrtz_f16_f32 v14, v68, v70
	v_cvt_pkrtz_f16_f32 v15, v72, v74
	v_cvt_pkrtz_f16_f32 v16, v61, v63
	v_cvt_pkrtz_f16_f32 v17, v65, v67
	v_cvt_pkrtz_f16_f32 v18, v69, v71
	v_cvt_pkrtz_f16_f32 v19, v73, v75
	s_mov_b32 s40, 0xb430
	s_mov_b32 s41, 0x2d0c0
	s_mov_b32 s42, 0x4ed50
	s_mov_b32 s43, 0x709e0
	s_mov_b32 s44, 0x92670
	s_mov_b32 s45, 0xb4300
	s_mov_b32 s46, 0xd5f90
	s_mov_b32 s47, 0xf7c20
	buffer_load_dwordx2 v[44:45], v3, s[4:7], s40 offen nt
	buffer_load_dwordx2 v[46:47], v3, s[4:7], s41 offen nt
	buffer_load_dwordx2 v[48:49], v3, s[4:7], s42 offen nt
	buffer_load_dwordx2 v[50:51], v3, s[4:7], s43 offen nt
	buffer_load_dwordx2 v[52:53], v3, s[4:7], s44 offen nt
	buffer_load_dwordx2 v[54:55], v3, s[4:7], s45 offen nt
	buffer_load_dwordx2 v[56:57], v3, s[4:7], s46 offen nt
	buffer_load_dwordx2 v[58:59], v3, s[4:7], s47 offen nt
	ds_write_b128 v5, v[12:15] offset:256
	ds_write_b128 v5, v[16:19] offset:2304
	s_waitcnt vmcnt(16)
	v_cvt_pkrtz_f16_f32 v12, v76, v78
	v_cvt_pkrtz_f16_f32 v13, v80, v82
	v_cvt_pkrtz_f16_f32 v14, v84, v86
	v_cvt_pkrtz_f16_f32 v15, v88, v90
	v_cvt_pkrtz_f16_f32 v16, v77, v79
	v_cvt_pkrtz_f16_f32 v17, v81, v83
	v_cvt_pkrtz_f16_f32 v18, v85, v87
	v_cvt_pkrtz_f16_f32 v19, v89, v91
	s_mov_b32 s40, 0x1198b0
	s_mov_b32 s41, 0x13b540
	s_mov_b32 s42, 0x15d1d0
	s_mov_b32 s43, 0x17ee60
	s_mov_b32 s44, 0x1a0af0
	s_mov_b32 s45, 0x1c2780
	s_mov_b32 s46, 0x1e4410
	s_mov_b32 s47, 0x2060a0
	buffer_load_dwordx2 v[60:61], v3, s[4:7], s40 offen nt
	buffer_load_dwordx2 v[62:63], v3, s[4:7], s41 offen nt
	buffer_load_dwordx2 v[64:65], v3, s[4:7], s42 offen nt
	buffer_load_dwordx2 v[66:67], v3, s[4:7], s43 offen nt
	buffer_load_dwordx2 v[68:69], v3, s[4:7], s44 offen nt
	buffer_load_dwordx2 v[70:71], v3, s[4:7], s45 offen nt
	buffer_load_dwordx2 v[72:73], v3, s[4:7], s46 offen nt
	buffer_load_dwordx2 v[74:75], v3, s[4:7], s47 offen nt
	ds_write_b128 v5, v[12:15] offset:512
	ds_write_b128 v5, v[16:19] offset:2560
	s_waitcnt vmcnt(16)
	v_cvt_pkrtz_f16_f32 v12, v92, v94
	v_cvt_pkrtz_f16_f32 v13, v96, v98
	v_cvt_pkrtz_f16_f32 v14, v100, v102
	v_cvt_pkrtz_f16_f32 v15, v104, v106
	v_cvt_pkrtz_f16_f32 v16, v93, v95
	v_cvt_pkrtz_f16_f32 v17, v97, v99
	v_cvt_pkrtz_f16_f32 v18, v101, v103
	v_cvt_pkrtz_f16_f32 v19, v105, v107
	s_mov_b32 s40, 0x227d30
	s_mov_b32 s41, 0x2499c0
	s_mov_b32 s42, 0x26b650
	s_mov_b32 s43, 0x28d2e0
	s_mov_b32 s44, 0x2aef70
	s_mov_b32 s45, 0x2d0c00
	s_mov_b32 s46, 0x2f2890
	s_mov_b32 s47, 0x314520
	buffer_load_dwordx2 v[76:77], v3, s[4:7], s40 offen nt
	buffer_load_dwordx2 v[78:79], v3, s[4:7], s41 offen nt
	buffer_load_dwordx2 v[80:81], v3, s[4:7], s42 offen nt
	buffer_load_dwordx2 v[82:83], v3, s[4:7], s43 offen nt
	buffer_load_dwordx2 v[84:85], v3, s[4:7], s44 offen nt
	buffer_load_dwordx2 v[86:87], v3, s[4:7], s45 offen nt
	buffer_load_dwordx2 v[88:89], v3, s[4:7], s46 offen nt
	buffer_load_dwordx2 v[90:91], v3, s[4:7], s47 offen nt
	ds_write_b128 v5, v[12:15] offset:768
	ds_write_b128 v5, v[16:19] offset:2816
	s_waitcnt lgkmcnt(0)
	s_barrier
	ds_read_b128 v[12:15], v6 offset:0
	ds_read_b128 v[16:19], v6 offset:2048
	ds_read_b128 v[20:23], v7 offset:0
	ds_read_b128 v[24:27], v7 offset:2048
	ds_read_b128 v[28:31], v8 offset:0
	ds_read_b128 v[32:35], v8 offset:2048
	ds_read_b128 v[36:39], v9 offset:0
	ds_read_b128 v[40:43], v9 offset:2048
	s_waitcnt lgkmcnt(7)
	v_mfma_f32_16x16x32_f16 v[188:191], v[116:119], v[12:15], v[188:191]
	v_mfma_f32_16x16x32_f16 v[220:223], v[156:159], v[12:15], v[220:223]
	s_waitcnt lgkmcnt(6)
	v_mfma_f32_16x16x32_f16 v[192:195], v[120:123], v[16:19], v[192:195]
	v_mfma_f32_16x16x32_f16 v[224:227], v[160:163], v[16:19], v[224:227]
	s_waitcnt lgkmcnt(5)
	v_mfma_f32_16x16x32_f16 v[196:199], v[124:127], v[20:23], v[196:199]
	v_mfma_f32_16x16x32_f16 v[228:231], v[164:167], v[20:23], v[228:231]
	s_waitcnt lgkmcnt(4)
	v_mfma_f32_16x16x32_f16 v[200:203], v[128:131], v[24:27], v[200:203]
	v_mfma_f32_16x16x32_f16 v[232:235], v[168:171], v[24:27], v[232:235]
	s_waitcnt lgkmcnt(3)
	v_mfma_f32_16x16x32_f16 v[204:207], v[132:135], v[28:31], v[204:207]
	v_mfma_f32_16x16x32_f16 v[236:239], v[172:175], v[28:31], v[236:239]
	s_waitcnt lgkmcnt(2)
	v_mfma_f32_16x16x32_f16 v[208:211], v[136:139], v[32:35], v[208:211]
	v_mfma_f32_16x16x32_f16 v[240:243], v[176:179], v[32:35], v[240:243]
	s_waitcnt lgkmcnt(1)
	v_mfma_f32_16x16x32_f16 v[212:215], v[140:143], v[36:39], v[212:215]
	v_mfma_f32_16x16x32_f16 v[244:247], v[180:183], v[36:39], v[244:247]
	s_waitcnt lgkmcnt(0)
	v_mfma_f32_16x16x32_f16 v[216:219], v[144:147], v[40:43], v[216:219]
	v_mfma_f32_16x16x32_f16 v[248:251], v[184:187], v[40:43], v[248:251]
	s_mov_b32 s40, 0x20000
	s_mov_b32 s41, 0x20400
	s_mov_b32 s42, 0x20800
	s_mov_b32 s43, 0x20c00
	buffer_load_dwordx4 v[108:111], v4, s[8:11], s40 offen
	buffer_load_dwordx4 v[112:115], v4, s[8:11], s41 offen
	buffer_load_dwordx4 v[116:119], v4, s[8:11], s42 offen
	buffer_load_dwordx4 v[120:123], v4, s[8:11], s43 offen
	s_mov_b32 s40, 0x21000
	s_mov_b32 s41, 0x21400
	s_mov_b32 s42, 0x21800
	s_mov_b32 s43, 0x21c00
	buffer_load_dwordx4 v[124:127], v4, s[8:11], s40 offen
	buffer_load_dwordx4 v[128:131], v4, s[8:11], s41 offen
	buffer_load_dwordx4 v[132:135], v4, s[8:11], s42 offen
	buffer_load_dwordx4 v[136:139], v4, s[8:11], s43 offen
	s_mov_b32 s40, 0x3361b0
	s_mov_b32 s41, 0x357e40
	s_mov_b32 s42, 0x379ad0
	s_mov_b32 s43, 0x39b760
	s_mov_b32 s44, 0x3bd3f0
	s_mov_b32 s45, 0x3df080
	s_mov_b32 s46, 0x400d10
	s_mov_b32 s47, 0x4229a0
	buffer_load_dwordx2 v[92:93], v3, s[4:7], s40 offen nt
	buffer_load_dwordx2 v[94:95], v3, s[4:7], s41 offen nt
	buffer_load_dwordx2 v[96:97], v3, s[4:7], s42 offen nt
	buffer_load_dwordx2 v[98:99], v3, s[4:7], s43 offen nt
	buffer_load_dwordx2 v[100:101], v3, s[4:7], s44 offen nt
	buffer_load_dwordx2 v[102:103], v3, s[4:7], s45 offen nt
	buffer_load_dwordx2 v[104:105], v3, s[4:7], s46 offen nt
	buffer_load_dwordx2 v[106:107], v3, s[4:7], s47 offen nt
	s_waitcnt vmcnt(32)
	v_cvt_pkrtz_f16_f32 v12, v44, v46
	v_cvt_pkrtz_f16_f32 v13, v48, v50
	v_cvt_pkrtz_f16_f32 v14, v52, v54
	v_cvt_pkrtz_f16_f32 v15, v56, v58
	v_cvt_pkrtz_f16_f32 v16, v45, v47
	v_cvt_pkrtz_f16_f32 v17, v49, v51
	v_cvt_pkrtz_f16_f32 v18, v53, v55
	v_cvt_pkrtz_f16_f32 v19, v57, v59
	ds_write_b128 v5, v[12:15] offset:1024
	ds_write_b128 v5, v[16:19] offset:3072
	s_waitcnt vmcnt(24)
	v_cvt_pkrtz_f16_f32 v12, v60, v62
	v_cvt_pkrtz_f16_f32 v13, v64, v66
	v_cvt_pkrtz_f16_f32 v14, v68, v70
	v_cvt_pkrtz_f16_f32 v15, v72, v74
	v_cvt_pkrtz_f16_f32 v16, v61, v63
	v_cvt_pkrtz_f16_f32 v17, v65, v67
	v_cvt_pkrtz_f16_f32 v18, v69, v71
	v_cvt_pkrtz_f16_f32 v19, v73, v75
	s_mov_b32 s40, 0xf040
	s_mov_b32 s41, 0x30cd0
	s_mov_b32 s42, 0x52960
	s_mov_b32 s43, 0x745f0
	s_mov_b32 s44, 0x96280
	s_mov_b32 s45, 0xb7f10
	s_mov_b32 s46, 0xd9ba0
	s_mov_b32 s47, 0xfb830
	buffer_load_dwordx2 v[44:45], v3, s[4:7], s40 offen nt
	buffer_load_dwordx2 v[46:47], v3, s[4:7], s41 offen nt
	buffer_load_dwordx2 v[48:49], v3, s[4:7], s42 offen nt
	buffer_load_dwordx2 v[50:51], v3, s[4:7], s43 offen nt
	buffer_load_dwordx2 v[52:53], v3, s[4:7], s44 offen nt
	buffer_load_dwordx2 v[54:55], v3, s[4:7], s45 offen nt
	buffer_load_dwordx2 v[56:57], v3, s[4:7], s46 offen nt
	buffer_load_dwordx2 v[58:59], v3, s[4:7], s47 offen nt
	ds_write_b128 v5, v[12:15] offset:1280
	ds_write_b128 v5, v[16:19] offset:3328
	s_waitcnt vmcnt(24)
	v_cvt_pkrtz_f16_f32 v12, v76, v78
	v_cvt_pkrtz_f16_f32 v13, v80, v82
	v_cvt_pkrtz_f16_f32 v14, v84, v86
	v_cvt_pkrtz_f16_f32 v15, v88, v90
	v_cvt_pkrtz_f16_f32 v16, v77, v79
	v_cvt_pkrtz_f16_f32 v17, v81, v83
	v_cvt_pkrtz_f16_f32 v18, v85, v87
	v_cvt_pkrtz_f16_f32 v19, v89, v91
	s_mov_b32 s40, 0x11d4c0
	s_mov_b32 s41, 0x13f150
	s_mov_b32 s42, 0x160de0
	s_mov_b32 s43, 0x182a70
	s_mov_b32 s44, 0x1a4700
	s_mov_b32 s45, 0x1c6390
	s_mov_b32 s46, 0x1e8020
	s_mov_b32 s47, 0x209cb0
	buffer_load_dwordx2 v[60:61], v3, s[4:7], s40 offen nt
	buffer_load_dwordx2 v[62:63], v3, s[4:7], s41 offen nt
	buffer_load_dwordx2 v[64:65], v3, s[4:7], s42 offen nt
	buffer_load_dwordx2 v[66:67], v3, s[4:7], s43 offen nt
	buffer_load_dwordx2 v[68:69], v3, s[4:7], s44 offen nt
	buffer_load_dwordx2 v[70:71], v3, s[4:7], s45 offen nt
	buffer_load_dwordx2 v[72:73], v3, s[4:7], s46 offen nt
	buffer_load_dwordx2 v[74:75], v3, s[4:7], s47 offen nt
	ds_write_b128 v5, v[12:15] offset:1536
	ds_write_b128 v5, v[16:19] offset:3584
	s_waitcnt vmcnt(16)
	v_cvt_pkrtz_f16_f32 v12, v92, v94
	v_cvt_pkrtz_f16_f32 v13, v96, v98
	v_cvt_pkrtz_f16_f32 v14, v100, v102
	v_cvt_pkrtz_f16_f32 v15, v104, v106
	v_cvt_pkrtz_f16_f32 v16, v93, v95
	v_cvt_pkrtz_f16_f32 v17, v97, v99
	v_cvt_pkrtz_f16_f32 v18, v101, v103
	v_cvt_pkrtz_f16_f32 v19, v105, v107
	s_mov_b32 s40, 0x22b940
	s_mov_b32 s41, 0x24d5d0
	s_mov_b32 s42, 0x26f260
	s_mov_b32 s43, 0x290ef0
	s_mov_b32 s44, 0x2b2b80
	s_mov_b32 s45, 0x2d4810
	s_mov_b32 s46, 0x2f64a0
	s_mov_b32 s47, 0x318130
	buffer_load_dwordx2 v[76:77], v3, s[4:7], s40 offen nt
	buffer_load_dwordx2 v[78:79], v3, s[4:7], s41 offen nt
	buffer_load_dwordx2 v[80:81], v3, s[4:7], s42 offen nt
	buffer_load_dwordx2 v[82:83], v3, s[4:7], s43 offen nt
	buffer_load_dwordx2 v[84:85], v3, s[4:7], s44 offen nt
	buffer_load_dwordx2 v[86:87], v3, s[4:7], s45 offen nt
	buffer_load_dwordx2 v[88:89], v3, s[4:7], s46 offen nt
	buffer_load_dwordx2 v[90:91], v3, s[4:7], s47 offen nt
	ds_write_b128 v5, v[12:15] offset:1792
	ds_write_b128 v5, v[16:19] offset:3840
	ds_write_b128 v254, v[108:111] offset:0
	ds_write_b128 v254, v[112:115] offset:1024
	s_waitcnt lgkmcnt(0)
	s_barrier
	ds_read_b128 v[140:143], v255 offset:0
	ds_read_b128 v[144:147], v255 offset:1024
	ds_read_b128 v[12:15], v6 offset:1024
	ds_read_b128 v[16:19], v6 offset:3072
	ds_read_b128 v[20:23], v7 offset:1024
	ds_read_b128 v[24:27], v7 offset:3072
	ds_read_b128 v[28:31], v8 offset:1024
	ds_read_b128 v[32:35], v8 offset:3072
	ds_read_b128 v[36:39], v9 offset:1024
	ds_read_b128 v[40:43], v9 offset:3072
	s_waitcnt lgkmcnt(7)
	v_mfma_f32_16x16x32_f16 v[188:191], v[148:151], v[12:15], v[188:191]
	v_mfma_f32_16x16x32_f16 v[220:223], v[108:111], v[12:15], v[220:223]
	s_waitcnt lgkmcnt(6)
	v_mfma_f32_16x16x32_f16 v[192:195], v[152:155], v[16:19], v[192:195]
	v_mfma_f32_16x16x32_f16 v[224:227], v[112:115], v[16:19], v[224:227]
	s_waitcnt lgkmcnt(5)
	v_mfma_f32_16x16x32_f16 v[196:199], v[156:159], v[20:23], v[196:199]
	v_mfma_f32_16x16x32_f16 v[228:231], v[116:119], v[20:23], v[228:231]
	s_waitcnt lgkmcnt(4)
	v_mfma_f32_16x16x32_f16 v[200:203], v[160:163], v[24:27], v[200:203]
	v_mfma_f32_16x16x32_f16 v[232:235], v[120:123], v[24:27], v[232:235]
	s_waitcnt lgkmcnt(3)
	v_mfma_f32_16x16x32_f16 v[204:207], v[164:167], v[28:31], v[204:207]
	v_mfma_f32_16x16x32_f16 v[236:239], v[124:127], v[28:31], v[236:239]
	s_waitcnt lgkmcnt(2)
	v_mfma_f32_16x16x32_f16 v[208:211], v[168:171], v[32:35], v[208:211]
	v_mfma_f32_16x16x32_f16 v[240:243], v[128:131], v[32:35], v[240:243]
	s_waitcnt lgkmcnt(1)
	v_mfma_f32_16x16x32_f16 v[212:215], v[172:175], v[36:39], v[212:215]
	v_mfma_f32_16x16x32_f16 v[244:247], v[132:135], v[36:39], v[244:247]
	s_waitcnt lgkmcnt(0)
	v_mfma_f32_16x16x32_f16 v[216:219], v[176:179], v[40:43], v[216:219]
	v_mfma_f32_16x16x32_f16 v[248:251], v[136:139], v[40:43], v[248:251]
	s_mov_b32 s40, 0x339dc0
	s_mov_b32 s41, 0x35ba50
	s_mov_b32 s42, 0x37d6e0
	s_mov_b32 s43, 0x39f370
	s_mov_b32 s44, 0x3c1000
	s_mov_b32 s45, 0x3e2c90
	s_mov_b32 s46, 0x404920
	s_mov_b32 s47, 0x4265b0
	buffer_load_dwordx2 v[92:93], v3, s[4:7], s40 offen nt
	buffer_load_dwordx2 v[94:95], v3, s[4:7], s41 offen nt
	buffer_load_dwordx2 v[96:97], v3, s[4:7], s42 offen nt
	buffer_load_dwordx2 v[98:99], v3, s[4:7], s43 offen nt
	buffer_load_dwordx2 v[100:101], v3, s[4:7], s44 offen nt
	buffer_load_dwordx2 v[102:103], v3, s[4:7], s45 offen nt
	buffer_load_dwordx2 v[104:105], v3, s[4:7], s46 offen nt
	buffer_load_dwordx2 v[106:107], v3, s[4:7], s47 offen nt
	s_waitcnt vmcnt(24)
	v_cvt_pkrtz_f16_f32 v12, v44, v46
	v_cvt_pkrtz_f16_f32 v13, v48, v50
	v_cvt_pkrtz_f16_f32 v14, v52, v54
	v_cvt_pkrtz_f16_f32 v15, v56, v58
	v_cvt_pkrtz_f16_f32 v16, v45, v47
	v_cvt_pkrtz_f16_f32 v17, v49, v51
	v_cvt_pkrtz_f16_f32 v18, v53, v55
	v_cvt_pkrtz_f16_f32 v19, v57, v59
	ds_write_b128 v5, v[12:15] offset:0
	ds_write_b128 v5, v[16:19] offset:2048
	s_waitcnt vmcnt(16)
	v_cvt_pkrtz_f16_f32 v12, v60, v62
	v_cvt_pkrtz_f16_f32 v13, v64, v66
	v_cvt_pkrtz_f16_f32 v14, v68, v70
	v_cvt_pkrtz_f16_f32 v15, v72, v74
	v_cvt_pkrtz_f16_f32 v16, v61, v63
	v_cvt_pkrtz_f16_f32 v17, v65, v67
	v_cvt_pkrtz_f16_f32 v18, v69, v71
	v_cvt_pkrtz_f16_f32 v19, v73, v75
	s_mov_b32 s40, 0x12c50
	s_mov_b32 s41, 0x348e0
	s_mov_b32 s42, 0x56570
	s_mov_b32 s43, 0x78200
	s_mov_b32 s44, 0x99e90
	s_mov_b32 s45, 0xbbb20
	s_mov_b32 s46, 0xdd7b0
	s_mov_b32 s47, 0xff440
	buffer_load_dwordx2 v[44:45], v3, s[4:7], s40 offen nt
	buffer_load_dwordx2 v[46:47], v3, s[4:7], s41 offen nt
	buffer_load_dwordx2 v[48:49], v3, s[4:7], s42 offen nt
	buffer_load_dwordx2 v[50:51], v3, s[4:7], s43 offen nt
	buffer_load_dwordx2 v[52:53], v3, s[4:7], s44 offen nt
	buffer_load_dwordx2 v[54:55], v3, s[4:7], s45 offen nt
	buffer_load_dwordx2 v[56:57], v3, s[4:7], s46 offen nt
	buffer_load_dwordx2 v[58:59], v3, s[4:7], s47 offen nt
	ds_write_b128 v5, v[12:15] offset:256
	ds_write_b128 v5, v[16:19] offset:2304
	s_waitcnt vmcnt(16)
	v_cvt_pkrtz_f16_f32 v12, v76, v78
	v_cvt_pkrtz_f16_f32 v13, v80, v82
	v_cvt_pkrtz_f16_f32 v14, v84, v86
	v_cvt_pkrtz_f16_f32 v15, v88, v90
	v_cvt_pkrtz_f16_f32 v16, v77, v79
	v_cvt_pkrtz_f16_f32 v17, v81, v83
	v_cvt_pkrtz_f16_f32 v18, v85, v87
	v_cvt_pkrtz_f16_f32 v19, v89, v91
	s_mov_b32 s40, 0x1210d0
	s_mov_b32 s41, 0x142d60
	s_mov_b32 s42, 0x1649f0
	s_mov_b32 s43, 0x186680
	s_mov_b32 s44, 0x1a8310
	s_mov_b32 s45, 0x1c9fa0
	s_mov_b32 s46, 0x1ebc30
	s_mov_b32 s47, 0x20d8c0
	buffer_load_dwordx2 v[60:61], v3, s[4:7], s40 offen nt
	buffer_load_dwordx2 v[62:63], v3, s[4:7], s41 offen nt
	buffer_load_dwordx2 v[64:65], v3, s[4:7], s42 offen nt
	buffer_load_dwordx2 v[66:67], v3, s[4:7], s43 offen nt
	buffer_load_dwordx2 v[68:69], v3, s[4:7], s44 offen nt
	buffer_load_dwordx2 v[70:71], v3, s[4:7], s45 offen nt
	buffer_load_dwordx2 v[72:73], v3, s[4:7], s46 offen nt
	buffer_load_dwordx2 v[74:75], v3, s[4:7], s47 offen nt
	ds_write_b128 v5, v[12:15] offset:512
	ds_write_b128 v5, v[16:19] offset:2560
	s_waitcnt vmcnt(16)
	v_cvt_pkrtz_f16_f32 v12, v92, v94
	v_cvt_pkrtz_f16_f32 v13, v96, v98
	v_cvt_pkrtz_f16_f32 v14, v100, v102
	v_cvt_pkrtz_f16_f32 v15, v104, v106
	v_cvt_pkrtz_f16_f32 v16, v93, v95
	v_cvt_pkrtz_f16_f32 v17, v97, v99
	v_cvt_pkrtz_f16_f32 v18, v101, v103
	v_cvt_pkrtz_f16_f32 v19, v105, v107
	s_mov_b32 s40, 0x22f550
	s_mov_b32 s41, 0x2511e0
	s_mov_b32 s42, 0x272e70
	s_mov_b32 s43, 0x294b00
	s_mov_b32 s44, 0x2b6790
	s_mov_b32 s45, 0x2d8420
	s_mov_b32 s46, 0x2fa0b0
	s_mov_b32 s47, 0x31bd40
	buffer_load_dwordx2 v[76:77], v3, s[4:7], s40 offen nt
	buffer_load_dwordx2 v[78:79], v3, s[4:7], s41 offen nt
	buffer_load_dwordx2 v[80:81], v3, s[4:7], s42 offen nt
	buffer_load_dwordx2 v[82:83], v3, s[4:7], s43 offen nt
	buffer_load_dwordx2 v[84:85], v3, s[4:7], s44 offen nt
	buffer_load_dwordx2 v[86:87], v3, s[4:7], s45 offen nt
	buffer_load_dwordx2 v[88:89], v3, s[4:7], s46 offen nt
	buffer_load_dwordx2 v[90:91], v3, s[4:7], s47 offen nt
	ds_write_b128 v5, v[12:15] offset:768
	ds_write_b128 v5, v[16:19] offset:2816
	s_waitcnt lgkmcnt(0)
	s_barrier
	ds_read_b128 v[12:15], v6 offset:0
	ds_read_b128 v[16:19], v6 offset:2048
	ds_read_b128 v[20:23], v7 offset:0
	ds_read_b128 v[24:27], v7 offset:2048
	ds_read_b128 v[28:31], v8 offset:0
	ds_read_b128 v[32:35], v8 offset:2048
	ds_read_b128 v[36:39], v9 offset:0
	ds_read_b128 v[40:43], v9 offset:2048
	s_waitcnt lgkmcnt(7)
	v_mfma_f32_16x16x32_f16 v[188:191], v[152:155], v[12:15], v[188:191]
	v_mfma_f32_16x16x32_f16 v[220:223], v[112:115], v[12:15], v[220:223]
	s_waitcnt lgkmcnt(6)
	v_mfma_f32_16x16x32_f16 v[192:195], v[156:159], v[16:19], v[192:195]
	v_mfma_f32_16x16x32_f16 v[224:227], v[116:119], v[16:19], v[224:227]
	s_waitcnt lgkmcnt(5)
	v_mfma_f32_16x16x32_f16 v[196:199], v[160:163], v[20:23], v[196:199]
	v_mfma_f32_16x16x32_f16 v[228:231], v[120:123], v[20:23], v[228:231]
	s_waitcnt lgkmcnt(4)
	v_mfma_f32_16x16x32_f16 v[200:203], v[164:167], v[24:27], v[200:203]
	v_mfma_f32_16x16x32_f16 v[232:235], v[124:127], v[24:27], v[232:235]
	s_waitcnt lgkmcnt(3)
	v_mfma_f32_16x16x32_f16 v[204:207], v[168:171], v[28:31], v[204:207]
	v_mfma_f32_16x16x32_f16 v[236:239], v[128:131], v[28:31], v[236:239]
	s_waitcnt lgkmcnt(2)
	v_mfma_f32_16x16x32_f16 v[208:211], v[172:175], v[32:35], v[208:211]
	v_mfma_f32_16x16x32_f16 v[240:243], v[132:135], v[32:35], v[240:243]
	s_waitcnt lgkmcnt(1)
	v_mfma_f32_16x16x32_f16 v[212:215], v[176:179], v[36:39], v[212:215]
	v_mfma_f32_16x16x32_f16 v[244:247], v[136:139], v[36:39], v[244:247]
	s_waitcnt lgkmcnt(0)
	v_mfma_f32_16x16x32_f16 v[216:219], v[180:183], v[40:43], v[216:219]
	v_mfma_f32_16x16x32_f16 v[248:251], v[140:143], v[40:43], v[248:251]
	s_mov_b32 s40, 0x33d9d0
	s_mov_b32 s41, 0x35f660
	s_mov_b32 s42, 0x3812f0
	s_mov_b32 s43, 0x3a2f80
	s_mov_b32 s44, 0x3c4c10
	s_mov_b32 s45, 0x3e68a0
	s_mov_b32 s46, 0x408530
	s_mov_b32 s47, 0x42a1c0
	buffer_load_dwordx2 v[92:93], v3, s[4:7], s40 offen nt
	buffer_load_dwordx2 v[94:95], v3, s[4:7], s41 offen nt
	buffer_load_dwordx2 v[96:97], v3, s[4:7], s42 offen nt
	buffer_load_dwordx2 v[98:99], v3, s[4:7], s43 offen nt
	buffer_load_dwordx2 v[100:101], v3, s[4:7], s44 offen nt
	buffer_load_dwordx2 v[102:103], v3, s[4:7], s45 offen nt
	buffer_load_dwordx2 v[104:105], v3, s[4:7], s46 offen nt
	buffer_load_dwordx2 v[106:107], v3, s[4:7], s47 offen nt
	s_waitcnt vmcnt(24)
	v_cvt_pkrtz_f16_f32 v12, v44, v46
	v_cvt_pkrtz_f16_f32 v13, v48, v50
	v_cvt_pkrtz_f16_f32 v14, v52, v54
	v_cvt_pkrtz_f16_f32 v15, v56, v58
	v_cvt_pkrtz_f16_f32 v16, v45, v47
	v_cvt_pkrtz_f16_f32 v17, v49, v51
	v_cvt_pkrtz_f16_f32 v18, v53, v55
	v_cvt_pkrtz_f16_f32 v19, v57, v59
	ds_write_b128 v5, v[12:15] offset:1024
	ds_write_b128 v5, v[16:19] offset:3072
	s_waitcnt vmcnt(16)
	v_cvt_pkrtz_f16_f32 v12, v60, v62
	v_cvt_pkrtz_f16_f32 v13, v64, v66
	v_cvt_pkrtz_f16_f32 v14, v68, v70
	v_cvt_pkrtz_f16_f32 v15, v72, v74
	v_cvt_pkrtz_f16_f32 v16, v61, v63
	v_cvt_pkrtz_f16_f32 v17, v65, v67
	v_cvt_pkrtz_f16_f32 v18, v69, v71
	v_cvt_pkrtz_f16_f32 v19, v73, v75
	s_mov_b32 s40, 0x16860
	s_mov_b32 s41, 0x384f0
	s_mov_b32 s42, 0x5a180
	s_mov_b32 s43, 0x7be10
	s_mov_b32 s44, 0x9daa0
	s_mov_b32 s45, 0xbf730
	s_mov_b32 s46, 0xe13c0
	s_mov_b32 s47, 0x103050
	buffer_load_dwordx2 v[44:45], v3, s[4:7], s40 offen nt
	buffer_load_dwordx2 v[46:47], v3, s[4:7], s41 offen nt
	buffer_load_dwordx2 v[48:49], v3, s[4:7], s42 offen nt
	buffer_load_dwordx2 v[50:51], v3, s[4:7], s43 offen nt
	buffer_load_dwordx2 v[52:53], v3, s[4:7], s44 offen nt
	buffer_load_dwordx2 v[54:55], v3, s[4:7], s45 offen nt
	buffer_load_dwordx2 v[56:57], v3, s[4:7], s46 offen nt
	buffer_load_dwordx2 v[58:59], v3, s[4:7], s47 offen nt
	ds_write_b128 v5, v[12:15] offset:1280
	ds_write_b128 v5, v[16:19] offset:3328
	s_waitcnt vmcnt(16)
	v_cvt_pkrtz_f16_f32 v12, v76, v78
	v_cvt_pkrtz_f16_f32 v13, v80, v82
	v_cvt_pkrtz_f16_f32 v14, v84, v86
	v_cvt_pkrtz_f16_f32 v15, v88, v90
	v_cvt_pkrtz_f16_f32 v16, v77, v79
	v_cvt_pkrtz_f16_f32 v17, v81, v83
	v_cvt_pkrtz_f16_f32 v18, v85, v87
	v_cvt_pkrtz_f16_f32 v19, v89, v91
	s_mov_b32 s40, 0x124ce0
	s_mov_b32 s41, 0x146970
	s_mov_b32 s42, 0x168600
	s_mov_b32 s43, 0x18a290
	s_mov_b32 s44, 0x1abf20
	s_mov_b32 s45, 0x1cdbb0
	s_mov_b32 s46, 0x1ef840
	s_mov_b32 s47, 0x2114d0
	buffer_load_dwordx2 v[60:61], v3, s[4:7], s40 offen nt
	buffer_load_dwordx2 v[62:63], v3, s[4:7], s41 offen nt
	buffer_load_dwordx2 v[64:65], v3, s[4:7], s42 offen nt
	buffer_load_dwordx2 v[66:67], v3, s[4:7], s43 offen nt
	buffer_load_dwordx2 v[68:69], v3, s[4:7], s44 offen nt
	buffer_load_dwordx2 v[70:71], v3, s[4:7], s45 offen nt
	buffer_load_dwordx2 v[72:73], v3, s[4:7], s46 offen nt
	buffer_load_dwordx2 v[74:75], v3, s[4:7], s47 offen nt
	ds_write_b128 v5, v[12:15] offset:1536
	ds_write_b128 v5, v[16:19] offset:3584
	s_waitcnt vmcnt(16)
	v_cvt_pkrtz_f16_f32 v12, v92, v94
	v_cvt_pkrtz_f16_f32 v13, v96, v98
	v_cvt_pkrtz_f16_f32 v14, v100, v102
	v_cvt_pkrtz_f16_f32 v15, v104, v106
	v_cvt_pkrtz_f16_f32 v16, v93, v95
	v_cvt_pkrtz_f16_f32 v17, v97, v99
	v_cvt_pkrtz_f16_f32 v18, v101, v103
	v_cvt_pkrtz_f16_f32 v19, v105, v107
	s_mov_b32 s40, 0x233160
	s_mov_b32 s41, 0x254df0
	s_mov_b32 s42, 0x276a80
	s_mov_b32 s43, 0x298710
	s_mov_b32 s44, 0x2ba3a0
	s_mov_b32 s45, 0x2dc030
	s_mov_b32 s46, 0x2fdcc0
	s_mov_b32 s47, 0x31f950
	buffer_load_dwordx2 v[76:77], v3, s[4:7], s40 offen nt
	buffer_load_dwordx2 v[78:79], v3, s[4:7], s41 offen nt
	buffer_load_dwordx2 v[80:81], v3, s[4:7], s42 offen nt
	buffer_load_dwordx2 v[82:83], v3, s[4:7], s43 offen nt
	buffer_load_dwordx2 v[84:85], v3, s[4:7], s44 offen nt
	buffer_load_dwordx2 v[86:87], v3, s[4:7], s45 offen nt
	buffer_load_dwordx2 v[88:89], v3, s[4:7], s46 offen nt
	buffer_load_dwordx2 v[90:91], v3, s[4:7], s47 offen nt
	ds_write_b128 v5, v[12:15] offset:1792
	ds_write_b128 v5, v[16:19] offset:3840
	s_waitcnt lgkmcnt(0)
	s_barrier
	ds_read_b128 v[12:15], v6 offset:1024
	ds_read_b128 v[16:19], v6 offset:3072
	ds_read_b128 v[20:23], v7 offset:1024
	ds_read_b128 v[24:27], v7 offset:3072
	ds_read_b128 v[28:31], v8 offset:1024
	ds_read_b128 v[32:35], v8 offset:3072
	ds_read_b128 v[36:39], v9 offset:1024
	ds_read_b128 v[40:43], v9 offset:3072
	s_waitcnt lgkmcnt(7)
	v_mfma_f32_16x16x32_f16 v[188:191], v[156:159], v[12:15], v[188:191]
	v_mfma_f32_16x16x32_f16 v[220:223], v[116:119], v[12:15], v[220:223]
	s_waitcnt lgkmcnt(6)
	v_mfma_f32_16x16x32_f16 v[192:195], v[160:163], v[16:19], v[192:195]
	v_mfma_f32_16x16x32_f16 v[224:227], v[120:123], v[16:19], v[224:227]
	s_waitcnt lgkmcnt(5)
	v_mfma_f32_16x16x32_f16 v[196:199], v[164:167], v[20:23], v[196:199]
	v_mfma_f32_16x16x32_f16 v[228:231], v[124:127], v[20:23], v[228:231]
	s_waitcnt lgkmcnt(4)
	v_mfma_f32_16x16x32_f16 v[200:203], v[168:171], v[24:27], v[200:203]
	v_mfma_f32_16x16x32_f16 v[232:235], v[128:131], v[24:27], v[232:235]
	s_waitcnt lgkmcnt(3)
	v_mfma_f32_16x16x32_f16 v[204:207], v[172:175], v[28:31], v[204:207]
	v_mfma_f32_16x16x32_f16 v[236:239], v[132:135], v[28:31], v[236:239]
	s_waitcnt lgkmcnt(2)
	v_mfma_f32_16x16x32_f16 v[208:211], v[176:179], v[32:35], v[208:211]
	v_mfma_f32_16x16x32_f16 v[240:243], v[136:139], v[32:35], v[240:243]
	s_waitcnt lgkmcnt(1)
	v_mfma_f32_16x16x32_f16 v[212:215], v[180:183], v[36:39], v[212:215]
	v_mfma_f32_16x16x32_f16 v[244:247], v[140:143], v[36:39], v[244:247]
	s_waitcnt lgkmcnt(0)
	v_mfma_f32_16x16x32_f16 v[216:219], v[184:187], v[40:43], v[216:219]
	v_mfma_f32_16x16x32_f16 v[248:251], v[144:147], v[40:43], v[248:251]
	s_mov_b32 s40, 0x30000
	s_mov_b32 s41, 0x30400
	s_mov_b32 s42, 0x30800
	s_mov_b32 s43, 0x30c00
	buffer_load_dwordx4 v[148:151], v4, s[8:11], s40 offen
	buffer_load_dwordx4 v[152:155], v4, s[8:11], s41 offen
	buffer_load_dwordx4 v[156:159], v4, s[8:11], s42 offen
	buffer_load_dwordx4 v[160:163], v4, s[8:11], s43 offen
	s_mov_b32 s40, 0x31000
	s_mov_b32 s41, 0x31400
	s_mov_b32 s42, 0x31800
	s_mov_b32 s43, 0x31c00
	buffer_load_dwordx4 v[164:167], v4, s[8:11], s40 offen
	buffer_load_dwordx4 v[168:171], v4, s[8:11], s41 offen
	buffer_load_dwordx4 v[172:175], v4, s[8:11], s42 offen
	buffer_load_dwordx4 v[176:179], v4, s[8:11], s43 offen
	s_mov_b32 s40, 0x3415e0
	s_mov_b32 s41, 0x363270
	s_mov_b32 s42, 0x384f00
	s_mov_b32 s43, 0x3a6b90
	s_mov_b32 s44, 0x3c8820
	s_mov_b32 s45, 0x3ea4b0
	s_mov_b32 s46, 0x40c140
	s_mov_b32 s47, 0x42ddd0
	buffer_load_dwordx2 v[92:93], v3, s[4:7], s40 offen nt
	buffer_load_dwordx2 v[94:95], v3, s[4:7], s41 offen nt
	buffer_load_dwordx2 v[96:97], v3, s[4:7], s42 offen nt
	buffer_load_dwordx2 v[98:99], v3, s[4:7], s43 offen nt
	buffer_load_dwordx2 v[100:101], v3, s[4:7], s44 offen nt
	buffer_load_dwordx2 v[102:103], v3, s[4:7], s45 offen nt
	buffer_load_dwordx2 v[104:105], v3, s[4:7], s46 offen nt
	buffer_load_dwordx2 v[106:107], v3, s[4:7], s47 offen nt
	s_waitcnt vmcnt(32)
	v_cvt_pkrtz_f16_f32 v12, v44, v46
	v_cvt_pkrtz_f16_f32 v13, v48, v50
	v_cvt_pkrtz_f16_f32 v14, v52, v54
	v_cvt_pkrtz_f16_f32 v15, v56, v58
	v_cvt_pkrtz_f16_f32 v16, v45, v47
	v_cvt_pkrtz_f16_f32 v17, v49, v51
	v_cvt_pkrtz_f16_f32 v18, v53, v55
	v_cvt_pkrtz_f16_f32 v19, v57, v59
	ds_write_b128 v5, v[12:15] offset:0
	ds_write_b128 v5, v[16:19] offset:2048
	s_waitcnt vmcnt(24)
	v_cvt_pkrtz_f16_f32 v12, v60, v62
	v_cvt_pkrtz_f16_f32 v13, v64, v66
	v_cvt_pkrtz_f16_f32 v14, v68, v70
	v_cvt_pkrtz_f16_f32 v15, v72, v74
	v_cvt_pkrtz_f16_f32 v16, v61, v63
	v_cvt_pkrtz_f16_f32 v17, v65, v67
	v_cvt_pkrtz_f16_f32 v18, v69, v71
	v_cvt_pkrtz_f16_f32 v19, v73, v75
	s_mov_b32 s40, 0x1a470
	s_mov_b32 s41, 0x3c100
	s_mov_b32 s42, 0x5dd90
	s_mov_b32 s43, 0x7fa20
	s_mov_b32 s44, 0xa16b0
	s_mov_b32 s45, 0xc3340
	s_mov_b32 s46, 0xe4fd0
	s_mov_b32 s47, 0x106c60
	buffer_load_dwordx2 v[44:45], v3, s[4:7], s40 offen nt
	buffer_load_dwordx2 v[46:47], v3, s[4:7], s41 offen nt
	buffer_load_dwordx2 v[48:49], v3, s[4:7], s42 offen nt
	buffer_load_dwordx2 v[50:51], v3, s[4:7], s43 offen nt
	buffer_load_dwordx2 v[52:53], v3, s[4:7], s44 offen nt
	buffer_load_dwordx2 v[54:55], v3, s[4:7], s45 offen nt
	buffer_load_dwordx2 v[56:57], v3, s[4:7], s46 offen nt
	buffer_load_dwordx2 v[58:59], v3, s[4:7], s47 offen nt
	ds_write_b128 v5, v[12:15] offset:256
	ds_write_b128 v5, v[16:19] offset:2304
	s_waitcnt vmcnt(24)
	v_cvt_pkrtz_f16_f32 v12, v76, v78
	v_cvt_pkrtz_f16_f32 v13, v80, v82
	v_cvt_pkrtz_f16_f32 v14, v84, v86
	v_cvt_pkrtz_f16_f32 v15, v88, v90
	v_cvt_pkrtz_f16_f32 v16, v77, v79
	v_cvt_pkrtz_f16_f32 v17, v81, v83
	v_cvt_pkrtz_f16_f32 v18, v85, v87
	v_cvt_pkrtz_f16_f32 v19, v89, v91
	s_mov_b32 s40, 0x1288f0
	s_mov_b32 s41, 0x14a580
	s_mov_b32 s42, 0x16c210
	s_mov_b32 s43, 0x18dea0
	s_mov_b32 s44, 0x1afb30
	s_mov_b32 s45, 0x1d17c0
	s_mov_b32 s46, 0x1f3450
	s_mov_b32 s47, 0x2150e0
	buffer_load_dwordx2 v[60:61], v3, s[4:7], s40 offen nt
	buffer_load_dwordx2 v[62:63], v3, s[4:7], s41 offen nt
	buffer_load_dwordx2 v[64:65], v3, s[4:7], s42 offen nt
	buffer_load_dwordx2 v[66:67], v3, s[4:7], s43 offen nt
	buffer_load_dwordx2 v[68:69], v3, s[4:7], s44 offen nt
	buffer_load_dwordx2 v[70:71], v3, s[4:7], s45 offen nt
	buffer_load_dwordx2 v[72:73], v3, s[4:7], s46 offen nt
	buffer_load_dwordx2 v[74:75], v3, s[4:7], s47 offen nt
	ds_write_b128 v5, v[12:15] offset:512
	ds_write_b128 v5, v[16:19] offset:2560
	s_waitcnt vmcnt(16)
	v_cvt_pkrtz_f16_f32 v12, v92, v94
	v_cvt_pkrtz_f16_f32 v13, v96, v98
	v_cvt_pkrtz_f16_f32 v14, v100, v102
	v_cvt_pkrtz_f16_f32 v15, v104, v106
	v_cvt_pkrtz_f16_f32 v16, v93, v95
	v_cvt_pkrtz_f16_f32 v17, v97, v99
	v_cvt_pkrtz_f16_f32 v18, v101, v103
	v_cvt_pkrtz_f16_f32 v19, v105, v107
	s_mov_b32 s40, 0x236d70
	s_mov_b32 s41, 0x258a00
	s_mov_b32 s42, 0x27a690
	s_mov_b32 s43, 0x29c320
	s_mov_b32 s44, 0x2bdfb0
	s_mov_b32 s45, 0x2dfc40
	s_mov_b32 s46, 0x3018d0
	s_mov_b32 s47, 0x323560
	buffer_load_dwordx2 v[76:77], v3, s[4:7], s40 offen nt
	buffer_load_dwordx2 v[78:79], v3, s[4:7], s41 offen nt
	buffer_load_dwordx2 v[80:81], v3, s[4:7], s42 offen nt
	buffer_load_dwordx2 v[82:83], v3, s[4:7], s43 offen nt
	buffer_load_dwordx2 v[84:85], v3, s[4:7], s44 offen nt
	buffer_load_dwordx2 v[86:87], v3, s[4:7], s45 offen nt
	buffer_load_dwordx2 v[88:89], v3, s[4:7], s46 offen nt
	buffer_load_dwordx2 v[90:91], v3, s[4:7], s47 offen nt
	ds_write_b128 v5, v[12:15] offset:768
	ds_write_b128 v5, v[16:19] offset:2816
	ds_write_b128 v254, v[148:151] offset:16384
	ds_write_b128 v254, v[152:155] offset:17408
	s_waitcnt lgkmcnt(0)
	s_barrier
	ds_read_b128 v[180:183], v255 offset:16384
	ds_read_b128 v[184:187], v255 offset:17408
	ds_read_b128 v[12:15], v6 offset:0
	ds_read_b128 v[16:19], v6 offset:2048
	ds_read_b128 v[20:23], v7 offset:0
	ds_read_b128 v[24:27], v7 offset:2048
	ds_read_b128 v[28:31], v8 offset:0
	ds_read_b128 v[32:35], v8 offset:2048
	ds_read_b128 v[36:39], v9 offset:0
	ds_read_b128 v[40:43], v9 offset:2048
	s_waitcnt lgkmcnt(7)
	v_mfma_f32_16x16x32_f16 v[188:191], v[108:111], v[12:15], v[188:191]
	v_mfma_f32_16x16x32_f16 v[220:223], v[148:151], v[12:15], v[220:223]
	s_waitcnt lgkmcnt(6)
	v_mfma_f32_16x16x32_f16 v[192:195], v[112:115], v[16:19], v[192:195]
	v_mfma_f32_16x16x32_f16 v[224:227], v[152:155], v[16:19], v[224:227]
	s_waitcnt lgkmcnt(5)
	v_mfma_f32_16x16x32_f16 v[196:199], v[116:119], v[20:23], v[196:199]
	v_mfma_f32_16x16x32_f16 v[228:231], v[156:159], v[20:23], v[228:231]
	s_waitcnt lgkmcnt(4)
	v_mfma_f32_16x16x32_f16 v[200:203], v[120:123], v[24:27], v[200:203]
	v_mfma_f32_16x16x32_f16 v[232:235], v[160:163], v[24:27], v[232:235]
	s_waitcnt lgkmcnt(3)
	v_mfma_f32_16x16x32_f16 v[204:207], v[124:127], v[28:31], v[204:207]
	v_mfma_f32_16x16x32_f16 v[236:239], v[164:167], v[28:31], v[236:239]
	s_waitcnt lgkmcnt(2)
	v_mfma_f32_16x16x32_f16 v[208:211], v[128:131], v[32:35], v[208:211]
	v_mfma_f32_16x16x32_f16 v[240:243], v[168:171], v[32:35], v[240:243]
	s_waitcnt lgkmcnt(1)
	v_mfma_f32_16x16x32_f16 v[212:215], v[132:135], v[36:39], v[212:215]
	v_mfma_f32_16x16x32_f16 v[244:247], v[172:175], v[36:39], v[244:247]
	s_waitcnt lgkmcnt(0)
	v_mfma_f32_16x16x32_f16 v[216:219], v[136:139], v[40:43], v[216:219]
	v_mfma_f32_16x16x32_f16 v[248:251], v[176:179], v[40:43], v[248:251]
	s_mov_b32 s40, 0x3451f0
	s_mov_b32 s41, 0x366e80
	s_mov_b32 s42, 0x388b10
	s_mov_b32 s43, 0x3aa7a0
	s_mov_b32 s44, 0x3cc430
	s_mov_b32 s45, 0x3ee0c0
	s_mov_b32 s46, 0x40fd50
	s_mov_b32 s47, 0x4319e0
	buffer_load_dwordx2 v[92:93], v3, s[4:7], s40 offen nt
	buffer_load_dwordx2 v[94:95], v3, s[4:7], s41 offen nt
	buffer_load_dwordx2 v[96:97], v3, s[4:7], s42 offen nt
	buffer_load_dwordx2 v[98:99], v3, s[4:7], s43 offen nt
	buffer_load_dwordx2 v[100:101], v3, s[4:7], s44 offen nt
	buffer_load_dwordx2 v[102:103], v3, s[4:7], s45 offen nt
	buffer_load_dwordx2 v[104:105], v3, s[4:7], s46 offen nt
	buffer_load_dwordx2 v[106:107], v3, s[4:7], s47 offen nt
	s_waitcnt vmcnt(24)
	v_cvt_pkrtz_f16_f32 v12, v44, v46
	v_cvt_pkrtz_f16_f32 v13, v48, v50
	v_cvt_pkrtz_f16_f32 v14, v52, v54
	v_cvt_pkrtz_f16_f32 v15, v56, v58
	v_cvt_pkrtz_f16_f32 v16, v45, v47
	v_cvt_pkrtz_f16_f32 v17, v49, v51
	v_cvt_pkrtz_f16_f32 v18, v53, v55
	v_cvt_pkrtz_f16_f32 v19, v57, v59
	ds_write_b128 v5, v[12:15] offset:1024
	ds_write_b128 v5, v[16:19] offset:3072
	s_waitcnt vmcnt(16)
	v_cvt_pkrtz_f16_f32 v12, v60, v62
	v_cvt_pkrtz_f16_f32 v13, v64, v66
	v_cvt_pkrtz_f16_f32 v14, v68, v70
	v_cvt_pkrtz_f16_f32 v15, v72, v74
	v_cvt_pkrtz_f16_f32 v16, v61, v63
	v_cvt_pkrtz_f16_f32 v17, v65, v67
	v_cvt_pkrtz_f16_f32 v18, v69, v71
	v_cvt_pkrtz_f16_f32 v19, v73, v75
	s_mov_b32 s40, 0x1e080
	s_mov_b32 s41, 0x3fd10
	s_mov_b32 s42, 0x619a0
	s_mov_b32 s43, 0x83630
	s_mov_b32 s44, 0xa52c0
	s_mov_b32 s45, 0xc6f50
	s_mov_b32 s46, 0xe8be0
	s_mov_b32 s47, 0x10a870
	buffer_load_dwordx2 v[44:45], v3, s[4:7], s40 offen nt
	buffer_load_dwordx2 v[46:47], v3, s[4:7], s41 offen nt
	buffer_load_dwordx2 v[48:49], v3, s[4:7], s42 offen nt
	buffer_load_dwordx2 v[50:51], v3, s[4:7], s43 offen nt
	buffer_load_dwordx2 v[52:53], v3, s[4:7], s44 offen nt
	buffer_load_dwordx2 v[54:55], v3, s[4:7], s45 offen nt
	buffer_load_dwordx2 v[56:57], v3, s[4:7], s46 offen nt
	buffer_load_dwordx2 v[58:59], v3, s[4:7], s47 offen nt
	ds_write_b128 v5, v[12:15] offset:1280
	ds_write_b128 v5, v[16:19] offset:3328
	s_waitcnt vmcnt(16)
	v_cvt_pkrtz_f16_f32 v12, v76, v78
	v_cvt_pkrtz_f16_f32 v13, v80, v82
	v_cvt_pkrtz_f16_f32 v14, v84, v86
	v_cvt_pkrtz_f16_f32 v15, v88, v90
	v_cvt_pkrtz_f16_f32 v16, v77, v79
	v_cvt_pkrtz_f16_f32 v17, v81, v83
	v_cvt_pkrtz_f16_f32 v18, v85, v87
	v_cvt_pkrtz_f16_f32 v19, v89, v91
	s_mov_b32 s40, 0x12c500
	s_mov_b32 s41, 0x14e190
	s_mov_b32 s42, 0x16fe20
	s_mov_b32 s43, 0x191ab0
	s_mov_b32 s44, 0x1b3740
	s_mov_b32 s45, 0x1d53d0
	s_mov_b32 s46, 0x1f7060
	s_mov_b32 s47, 0x218cf0
	buffer_load_dwordx2 v[60:61], v3, s[4:7], s40 offen nt
	buffer_load_dwordx2 v[62:63], v3, s[4:7], s41 offen nt
	buffer_load_dwordx2 v[64:65], v3, s[4:7], s42 offen nt
	buffer_load_dwordx2 v[66:67], v3, s[4:7], s43 offen nt
	buffer_load_dwordx2 v[68:69], v3, s[4:7], s44 offen nt
	buffer_load_dwordx2 v[70:71], v3, s[4:7], s45 offen nt
	buffer_load_dwordx2 v[72:73], v3, s[4:7], s46 offen nt
	buffer_load_dwordx2 v[74:75], v3, s[4:7], s47 offen nt
	ds_write_b128 v5, v[12:15] offset:1536
	ds_write_b128 v5, v[16:19] offset:3584
	s_waitcnt vmcnt(16)
	v_cvt_pkrtz_f16_f32 v12, v92, v94
	v_cvt_pkrtz_f16_f32 v13, v96, v98
	v_cvt_pkrtz_f16_f32 v14, v100, v102
	v_cvt_pkrtz_f16_f32 v15, v104, v106
	v_cvt_pkrtz_f16_f32 v16, v93, v95
	v_cvt_pkrtz_f16_f32 v17, v97, v99
	v_cvt_pkrtz_f16_f32 v18, v101, v103
	v_cvt_pkrtz_f16_f32 v19, v105, v107
	s_mov_b32 s40, 0x23a980
	s_mov_b32 s41, 0x25c610
	s_mov_b32 s42, 0x27e2a0
	s_mov_b32 s43, 0x29ff30
	s_mov_b32 s44, 0x2c1bc0
	s_mov_b32 s45, 0x2e3850
	s_mov_b32 s46, 0x3054e0
	s_mov_b32 s47, 0x327170
	buffer_load_dwordx2 v[76:77], v3, s[4:7], s40 offen nt
	buffer_load_dwordx2 v[78:79], v3, s[4:7], s41 offen nt
	buffer_load_dwordx2 v[80:81], v3, s[4:7], s42 offen nt
	buffer_load_dwordx2 v[82:83], v3, s[4:7], s43 offen nt
	buffer_load_dwordx2 v[84:85], v3, s[4:7], s44 offen nt
	buffer_load_dwordx2 v[86:87], v3, s[4:7], s45 offen nt
	buffer_load_dwordx2 v[88:89], v3, s[4:7], s46 offen nt
	buffer_load_dwordx2 v[90:91], v3, s[4:7], s47 offen nt
	ds_write_b128 v5, v[12:15] offset:1792
	ds_write_b128 v5, v[16:19] offset:3840
	s_waitcnt lgkmcnt(0)
	s_barrier
	ds_read_b128 v[12:15], v6 offset:1024
	ds_read_b128 v[16:19], v6 offset:3072
	ds_read_b128 v[20:23], v7 offset:1024
	ds_read_b128 v[24:27], v7 offset:3072
	ds_read_b128 v[28:31], v8 offset:1024
	ds_read_b128 v[32:35], v8 offset:3072
	ds_read_b128 v[36:39], v9 offset:1024
	ds_read_b128 v[40:43], v9 offset:3072
	s_waitcnt lgkmcnt(7)
	v_mfma_f32_16x16x32_f16 v[188:191], v[112:115], v[12:15], v[188:191]
	v_mfma_f32_16x16x32_f16 v[220:223], v[152:155], v[12:15], v[220:223]
	s_waitcnt lgkmcnt(6)
	v_mfma_f32_16x16x32_f16 v[192:195], v[116:119], v[16:19], v[192:195]
	v_mfma_f32_16x16x32_f16 v[224:227], v[156:159], v[16:19], v[224:227]
	s_waitcnt lgkmcnt(5)
	v_mfma_f32_16x16x32_f16 v[196:199], v[120:123], v[20:23], v[196:199]
	v_mfma_f32_16x16x32_f16 v[228:231], v[160:163], v[20:23], v[228:231]
	s_waitcnt lgkmcnt(4)
	v_mfma_f32_16x16x32_f16 v[200:203], v[124:127], v[24:27], v[200:203]
	v_mfma_f32_16x16x32_f16 v[232:235], v[164:167], v[24:27], v[232:235]
	s_waitcnt lgkmcnt(3)
	v_mfma_f32_16x16x32_f16 v[204:207], v[128:131], v[28:31], v[204:207]
	v_mfma_f32_16x16x32_f16 v[236:239], v[168:171], v[28:31], v[236:239]
	s_waitcnt lgkmcnt(2)
	v_mfma_f32_16x16x32_f16 v[208:211], v[132:135], v[32:35], v[208:211]
	v_mfma_f32_16x16x32_f16 v[240:243], v[172:175], v[32:35], v[240:243]
	s_waitcnt lgkmcnt(1)
	v_mfma_f32_16x16x32_f16 v[212:215], v[136:139], v[36:39], v[212:215]
	v_mfma_f32_16x16x32_f16 v[244:247], v[176:179], v[36:39], v[244:247]
	s_waitcnt lgkmcnt(0)
	v_mfma_f32_16x16x32_f16 v[216:219], v[140:143], v[40:43], v[216:219]
	v_mfma_f32_16x16x32_f16 v[248:251], v[180:183], v[40:43], v[248:251]
	s_mov_b32 s40, 0x348e00
	s_mov_b32 s41, 0x36aa90
	s_mov_b32 s42, 0x38c720
	s_mov_b32 s43, 0x3ae3b0
	s_mov_b32 s44, 0x3d0040
	s_mov_b32 s45, 0x3f1cd0
	s_mov_b32 s46, 0x413960
	s_mov_b32 s47, 0x4355f0
	buffer_load_dwordx2 v[92:93], v3, s[4:7], s40 offen nt
	buffer_load_dwordx2 v[94:95], v3, s[4:7], s41 offen nt
	buffer_load_dwordx2 v[96:97], v3, s[4:7], s42 offen nt
	buffer_load_dwordx2 v[98:99], v3, s[4:7], s43 offen nt
	buffer_load_dwordx2 v[100:101], v3, s[4:7], s44 offen nt
	buffer_load_dwordx2 v[102:103], v3, s[4:7], s45 offen nt
	buffer_load_dwordx2 v[104:105], v3, s[4:7], s46 offen nt
	buffer_load_dwordx2 v[106:107], v3, s[4:7], s47 offen nt
	s_waitcnt vmcnt(24)
	v_cvt_pkrtz_f16_f32 v12, v44, v46
	v_cvt_pkrtz_f16_f32 v13, v48, v50
	v_cvt_pkrtz_f16_f32 v14, v52, v54
	v_cvt_pkrtz_f16_f32 v15, v56, v58
	v_cvt_pkrtz_f16_f32 v16, v45, v47
	v_cvt_pkrtz_f16_f32 v17, v49, v51
	v_cvt_pkrtz_f16_f32 v18, v53, v55
	v_cvt_pkrtz_f16_f32 v19, v57, v59
	ds_write_b128 v5, v[12:15] offset:0
	ds_write_b128 v5, v[16:19] offset:2048
	s_waitcnt vmcnt(16)
	v_cvt_pkrtz_f16_f32 v12, v60, v62
	v_cvt_pkrtz_f16_f32 v13, v64, v66
	v_cvt_pkrtz_f16_f32 v14, v68, v70
	v_cvt_pkrtz_f16_f32 v15, v72, v74
	v_cvt_pkrtz_f16_f32 v16, v61, v63
	v_cvt_pkrtz_f16_f32 v17, v65, v67
	v_cvt_pkrtz_f16_f32 v18, v69, v71
	v_cvt_pkrtz_f16_f32 v19, v73, v75
	ds_write_b128 v5, v[12:15] offset:256
	ds_write_b128 v5, v[16:19] offset:2304
	s_waitcnt vmcnt(8)
	v_cvt_pkrtz_f16_f32 v12, v76, v78
	v_cvt_pkrtz_f16_f32 v13, v80, v82
	v_cvt_pkrtz_f16_f32 v14, v84, v86
	v_cvt_pkrtz_f16_f32 v15, v88, v90
	v_cvt_pkrtz_f16_f32 v16, v77, v79
	v_cvt_pkrtz_f16_f32 v17, v81, v83
	v_cvt_pkrtz_f16_f32 v18, v85, v87
	v_cvt_pkrtz_f16_f32 v19, v89, v91
	ds_write_b128 v5, v[12:15] offset:512
	ds_write_b128 v5, v[16:19] offset:2560
	s_waitcnt vmcnt(0)
	v_cvt_pkrtz_f16_f32 v12, v92, v94
	v_cvt_pkrtz_f16_f32 v13, v96, v98
	v_cvt_pkrtz_f16_f32 v14, v100, v102
	v_cvt_pkrtz_f16_f32 v15, v104, v106
	v_cvt_pkrtz_f16_f32 v16, v93, v95
	v_cvt_pkrtz_f16_f32 v17, v97, v99
	v_cvt_pkrtz_f16_f32 v18, v101, v103
	v_cvt_pkrtz_f16_f32 v19, v105, v107
	ds_write_b128 v5, v[12:15] offset:768
	ds_write_b128 v5, v[16:19] offset:2816
	s_waitcnt lgkmcnt(0)
	s_barrier
	ds_read_b128 v[12:15], v6 offset:0
	ds_read_b128 v[16:19], v6 offset:2048
	ds_read_b128 v[20:23], v7 offset:0
	ds_read_b128 v[24:27], v7 offset:2048
	ds_read_b128 v[28:31], v8 offset:0
	ds_read_b128 v[32:35], v8 offset:2048
	ds_read_b128 v[36:39], v9 offset:0
	ds_read_b128 v[40:43], v9 offset:2048
	s_waitcnt lgkmcnt(7)
	v_mfma_f32_16x16x32_f16 v[188:191], v[116:119], v[12:15], v[188:191]
	v_mfma_f32_16x16x32_f16 v[220:223], v[156:159], v[12:15], v[220:223]
	s_waitcnt lgkmcnt(6)
	v_mfma_f32_16x16x32_f16 v[192:195], v[120:123], v[16:19], v[192:195]
	v_mfma_f32_16x16x32_f16 v[224:227], v[160:163], v[16:19], v[224:227]
	s_waitcnt lgkmcnt(5)
	v_mfma_f32_16x16x32_f16 v[196:199], v[124:127], v[20:23], v[196:199]
	v_mfma_f32_16x16x32_f16 v[228:231], v[164:167], v[20:23], v[228:231]
	s_waitcnt lgkmcnt(4)
	v_mfma_f32_16x16x32_f16 v[200:203], v[128:131], v[24:27], v[200:203]
	v_mfma_f32_16x16x32_f16 v[232:235], v[168:171], v[24:27], v[232:235]
	s_waitcnt lgkmcnt(3)
	v_mfma_f32_16x16x32_f16 v[204:207], v[132:135], v[28:31], v[204:207]
	v_mfma_f32_16x16x32_f16 v[236:239], v[172:175], v[28:31], v[236:239]
	s_waitcnt lgkmcnt(2)
	v_mfma_f32_16x16x32_f16 v[208:211], v[136:139], v[32:35], v[208:211]
	v_mfma_f32_16x16x32_f16 v[240:243], v[176:179], v[32:35], v[240:243]
	s_waitcnt lgkmcnt(1)
	v_mfma_f32_16x16x32_f16 v[212:215], v[140:143], v[36:39], v[212:215]
	v_mfma_f32_16x16x32_f16 v[244:247], v[180:183], v[36:39], v[244:247]
	s_waitcnt lgkmcnt(0)
	v_mfma_f32_16x16x32_f16 v[216:219], v[144:147], v[40:43], v[216:219]
	v_mfma_f32_16x16x32_f16 v[248:251], v[184:187], v[40:43], v[248:251]
	s_nop 7
	s_nop 3
	v_and_b32_e32 v10, 1, v0
	v_cmp_eq_u32_e32 vcc, 1, v10
	s_nop 1
	v_cndmask_b32_e32 v188, v188, v220, vcc
	v_cndmask_b32_e32 v189, v189, v221, vcc
	v_cndmask_b32_e32 v190, v190, v222, vcc
	v_cndmask_b32_e32 v191, v191, v223, vcc
	v_cndmask_b32_e32 v192, v192, v224, vcc
	v_cndmask_b32_e32 v193, v193, v225, vcc
	v_cndmask_b32_e32 v194, v194, v226, vcc
	v_cndmask_b32_e32 v195, v195, v227, vcc
	v_cndmask_b32_e32 v196, v196, v228, vcc
	v_cndmask_b32_e32 v197, v197, v229, vcc
	v_cndmask_b32_e32 v198, v198, v230, vcc
	v_cndmask_b32_e32 v199, v199, v231, vcc
	v_cndmask_b32_e32 v200, v200, v232, vcc
	v_cndmask_b32_e32 v201, v201, v233, vcc
	v_cndmask_b32_e32 v202, v202, v234, vcc
	v_cndmask_b32_e32 v203, v203, v235, vcc
	v_cndmask_b32_e32 v204, v204, v236, vcc
	v_cndmask_b32_e32 v205, v205, v237, vcc
	v_cndmask_b32_e32 v206, v206, v238, vcc
	v_cndmask_b32_e32 v207, v207, v239, vcc
	v_cndmask_b32_e32 v208, v208, v240, vcc
	v_cndmask_b32_e32 v209, v209, v241, vcc
	v_cndmask_b32_e32 v210, v210, v242, vcc
	v_cndmask_b32_e32 v211, v211, v243, vcc
	v_cndmask_b32_e32 v212, v212, v244, vcc
	v_cndmask_b32_e32 v213, v213, v245, vcc
	v_cndmask_b32_e32 v214, v214, v246, vcc
	v_cndmask_b32_e32 v215, v215, v247, vcc
	v_cndmask_b32_e32 v216, v216, v248, vcc
	v_cndmask_b32_e32 v217, v217, v249, vcc
	v_cndmask_b32_e32 v218, v218, v250, vcc
	v_cndmask_b32_e32 v219, v219, v251, vcc
	s_barrier
	v_lshrrev_b32_e32 v10, 4, v2
	v_lshlrev_b32_e32 v10, 6, v10
	v_and_b32_e32 v12, 15, v2
	v_add_u32_e32 v10, v10, v12
	v_mul_u32_u24_e32 v10, 0x108, v10
	v_lshl_add_u32 v10, v1, 5, v10
	ds_write_b32 v10, v188 offset:0
	ds_write_b32 v10, v189 offset:4224
	ds_write_b32 v10, v190 offset:8448
	ds_write_b32 v10, v191 offset:12672
	ds_write_b32 v10, v192 offset:4
	ds_write_b32 v10, v193 offset:4228
	ds_write_b32 v10, v194 offset:8452
	ds_write_b32 v10, v195 offset:12676
	s_waitcnt lgkmcnt(4)
	ds_write_b32 v10, v196 offset:8
	ds_write_b32 v10, v197 offset:4232
	ds_write_b32 v10, v198 offset:8456
	ds_write_b32 v10, v199 offset:12680
	ds_write_b32 v10, v200 offset:12
	ds_write_b32 v10, v201 offset:4236
	ds_write_b32 v10, v202 offset:8460
	ds_write_b32 v10, v203 offset:12684
	s_waitcnt lgkmcnt(4)
	ds_write_b32 v10, v204 offset:16
	ds_write_b32 v10, v205 offset:4240
	ds_write_b32 v10, v206 offset:8464
	ds_write_b32 v10, v207 offset:12688
	ds_write_b32 v10, v208 offset:20
	ds_write_b32 v10, v209 offset:4244
	ds_write_b32 v10, v210 offset:8468
	ds_write_b32 v10, v211 offset:12692
	s_waitcnt lgkmcnt(4)
	ds_write_b32 v10, v212 offset:24
	ds_write_b32 v10, v213 offset:4248
	ds_write_b32 v10, v214 offset:8472
	ds_write_b32 v10, v215 offset:12696
	ds_write_b32 v10, v216 offset:28
	ds_write_b32 v10, v217 offset:4252
	ds_write_b32 v10, v218 offset:8476
	ds_write_b32 v10, v219 offset:12700
	s_waitcnt lgkmcnt(0)
	s_barrier
	v_lshrrev_b32_e32 v12, 5, v0
	v_mul_u32_u24_e32 v12, 0x108, v12
	v_and_b32_e32 v13, 31, v0
	v_lshl_add_u32 v12, v13, 3, v12
	ds_read_b64 v[44:45], v12 offset:0
	ds_read_b64 v[46:47], v12 offset:4224
	ds_read_b64 v[48:49], v12 offset:8448
	ds_read_b64 v[50:51], v12 offset:12672
	ds_read_b64 v[52:53], v12 offset:16896
	ds_read_b64 v[54:55], v12 offset:21120
	ds_read_b64 v[56:57], v12 offset:25344
	ds_read_b64 v[58:59], v12 offset:29568
	s_waitcnt lgkmcnt(7)
	v_add_f32_e32 v44, v252, v44
	v_add_f32_e32 v45, v253, v45
	s_mov_b32 s40, 0x0
	buffer_store_dwordx2 v[44:45], v11, s[32:35], s40 offen nt
	s_waitcnt lgkmcnt(6)
	v_add_f32_e32 v46, v252, v46
	v_add_f32_e32 v47, v253, v47
	s_mov_b32 s41, 0xf0400
	buffer_store_dwordx2 v[46:47], v11, s[32:35], s41 offen nt
	s_waitcnt lgkmcnt(5)
	v_add_f32_e32 v48, v252, v48
	v_add_f32_e32 v49, v253, v49
	s_mov_b32 s42, 0x1e0800
	buffer_store_dwordx2 v[48:49], v11, s[32:35], s42 offen nt
	s_waitcnt lgkmcnt(4)
	v_add_f32_e32 v50, v252, v50
	v_add_f32_e32 v51, v253, v51
	s_mov_b32 s43, 0x2d0c00
	buffer_store_dwordx2 v[50:51], v11, s[32:35], s43 offen nt
	s_waitcnt lgkmcnt(3)
	v_add_f32_e32 v52, v252, v52
	v_add_f32_e32 v53, v253, v53
	s_mov_b32 s44, 0x3c1000
	buffer_store_dwordx2 v[52:53], v11, s[32:35], s44 offen nt
	s_waitcnt lgkmcnt(2)
	v_add_f32_e32 v54, v252, v54
	v_add_f32_e32 v55, v253, v55
	s_mov_b32 s45, 0x4b1400
	buffer_store_dwordx2 v[54:55], v11, s[32:35], s45 offen nt
	s_waitcnt lgkmcnt(1)
	v_add_f32_e32 v56, v252, v56
	v_add_f32_e32 v57, v253, v57
	s_mov_b32 s46, 0x5a1800
	buffer_store_dwordx2 v[56:57], v11, s[32:35], s46 offen nt
	s_waitcnt lgkmcnt(0)
	v_add_f32_e32 v58, v252, v58
	v_add_f32_e32 v59, v253, v59
	s_mov_b32 s47, 0x691c00
	buffer_store_dwordx2 v[58:59], v11, s[32:35], s47 offen nt
	ds_read_b64 v[60:61], v12 offset:33792
	ds_read_b64 v[62:63], v12 offset:38016
	ds_read_b64 v[64:65], v12 offset:42240
	ds_read_b64 v[66:67], v12 offset:46464
	ds_read_b64 v[68:69], v12 offset:50688
	ds_read_b64 v[70:71], v12 offset:54912
	ds_read_b64 v[72:73], v12 offset:59136
	ds_read_b64 v[74:75], v12 offset:63360
	s_waitcnt lgkmcnt(7)
	v_add_f32_e32 v60, v252, v60
	v_add_f32_e32 v61, v253, v61
	s_mov_b32 s40, 0x782000
	buffer_store_dwordx2 v[60:61], v11, s[32:35], s40 offen nt
	s_waitcnt lgkmcnt(6)
	v_add_f32_e32 v62, v252, v62
	v_add_f32_e32 v63, v253, v63
	s_mov_b32 s41, 0x872400
	buffer_store_dwordx2 v[62:63], v11, s[32:35], s41 offen nt
	s_waitcnt lgkmcnt(5)
	v_add_f32_e32 v64, v252, v64
	v_add_f32_e32 v65, v253, v65
	s_mov_b32 s42, 0x962800
	buffer_store_dwordx2 v[64:65], v11, s[32:35], s42 offen nt
	s_waitcnt lgkmcnt(4)
	v_add_f32_e32 v66, v252, v66
	v_add_f32_e32 v67, v253, v67
	s_mov_b32 s43, 0xa52c00
	buffer_store_dwordx2 v[66:67], v11, s[32:35], s43 offen nt
	s_waitcnt lgkmcnt(3)
	v_add_f32_e32 v68, v252, v68
	v_add_f32_e32 v69, v253, v69
	s_mov_b32 s44, 0xb43000
	buffer_store_dwordx2 v[68:69], v11, s[32:35], s44 offen nt
	s_waitcnt lgkmcnt(2)
	v_add_f32_e32 v70, v252, v70
	v_add_f32_e32 v71, v253, v71
	s_mov_b32 s45, 0xc33400
	buffer_store_dwordx2 v[70:71], v11, s[32:35], s45 offen nt
	s_waitcnt lgkmcnt(1)
	v_add_f32_e32 v72, v252, v72
	v_add_f32_e32 v73, v253, v73
	s_mov_b32 s46, 0xd23800
	buffer_store_dwordx2 v[72:73], v11, s[32:35], s46 offen nt
	s_waitcnt lgkmcnt(0)
	v_add_f32_e32 v74, v252, v74
	v_add_f32_e32 v75, v253, v75
	s_mov_b32 s47, 0xe13c00
	buffer_store_dwordx2 v[74:75], v11, s[32:35], s47 offen nt
	s_endpgm
